# v048 + P11 tile fragment reads issued before the tile's LDS-DMA piece (tiles 1..24)
# baseline (speedup 1.0000x reference)
.LBB0_926:
	s_barrier
	ds_read_b128 v[2:5], v1 offset:8192
	ds_read_b128 v[18:21], v1 offset:12288
	ds_read_b128 v[94:97], v67 offset:8192
	ds_read_b128 v[228:231], v67 offset:12288
	ds_read_b128 v[232:235], v69 offset:8192
	ds_read_b128 v[236:239], v69 offset:12288
	ds_read_b128 v[240:243], v92 offset:8192
	ds_read_b128 v[244:247], v92 offset:12288
	s_cmp_lt_u32 s2, 16
	s_cbranch_scc1 .LBB0_928
	s_mov_b64 s[16:17], 0x10000
	v_lshl_add_u64 v[6:7], v[90:91], 0, s[16:17]
	s_mov_b32 m0, s24
	s_nop 0
	global_load_lds_dwordx4 v[6:7], off
.LBB0_928:
	s_waitcnt lgkmcnt(5)
	v_mfma_f32_32x32x16_bf16 v[2:17], v[62:65], v[2:5], 0
	v_mfma_f32_32x32x16_bf16 v[18:33], v[62:65], v[18:21], 0
	v_mfma_f32_32x32x16_bf16 v[2:17], v[58:61], v[94:97], v[2:17]
	s_waitcnt lgkmcnt(4)
	v_mfma_f32_32x32x16_bf16 v[18:33], v[58:61], v[228:231], v[18:33]
	s_waitcnt lgkmcnt(3)
	v_mfma_f32_32x32x16_bf16 v[2:17], v[54:57], v[232:235], v[2:17]
	s_waitcnt lgkmcnt(2)
	v_mfma_f32_32x32x16_bf16 v[18:33], v[54:57], v[236:239], v[18:33]
	s_waitcnt lgkmcnt(1)
	v_mfma_f32_32x32x16_bf16 v[2:17], v[50:53], v[240:243], v[2:17]
	s_waitcnt lgkmcnt(0)
	v_mfma_f32_32x32x16_bf16 v[18:33], v[50:53], v[244:247], v[18:33]
	s_nop 9
	v_max_i32_e32 v98, 0, v2
	v_max_i32_e32 v96, 0, v10
	v_max_i32_e32 v2, 0, v3
	v_max_i32_e32 v10, 0, v11
	v_max_i32_e32 v99, 0, v18
	v_pk_fma_f32 v[94:95], v[74:75], v[98:99], 0 op_sel_hi:[1,1,0]
	v_max_i32_e32 v97, 0, v26
	v_max_i32_e32 v3, 0, v19
	v_pk_fma_f32 v[96:97], v[76:77], v[96:97], 0 op_sel_hi:[1,1,0]
	v_pk_fma_f32 v[2:3], v[46:47], v[2:3], v[94:95]
	v_max_i32_e32 v11, 0, v27
	v_max_i32_e32 v18, 0, v4
	v_max_i32_e32 v19, 0, v20
	v_pk_fma_f32 v[10:11], v[42:43], v[10:11], v[96:97]
	v_pk_fma_f32 v[2:3], v[78:79], v[18:19], v[2:3]
	v_max_i32_e32 v18, 0, v12
	v_max_i32_e32 v19, 0, v28
	v_max_i32_e32 v4, 0, v5
	v_max_i32_e32 v5, 0, v21
	v_pk_fma_f32 v[10:11], v[80:81], v[18:19], v[10:11]
	v_pk_fma_f32 v[2:3], v[48:49], v[4:5], v[2:3]
	v_max_i32_e32 v4, 0, v13
	v_max_i32_e32 v5, 0, v29
	v_pk_fma_f32 v[4:5], v[44:45], v[4:5], v[10:11]
	v_max_i32_e32 v10, 0, v6
	v_max_i32_e32 v11, 0, v22
	v_pk_fma_f32 v[2:3], v[82:83], v[10:11], v[2:3]
	v_max_i32_e32 v10, 0, v14
	v_max_i32_e32 v11, 0, v30
	v_max_i32_e32 v6, 0, v7
	v_max_i32_e32 v7, 0, v23
	v_pk_fma_f32 v[4:5], v[84:85], v[10:11], v[4:5]
	v_pk_fma_f32 v[2:3], v[38:39], v[6:7], v[2:3]
	v_max_i32_e32 v6, 0, v15
	v_max_i32_e32 v7, 0, v31
	v_pk_fma_f32 v[4:5], v[34:35], v[6:7], v[4:5]
	v_max_i32_e32 v6, 0, v8
	v_max_i32_e32 v7, 0, v24
	v_pk_fma_f32 v[2:3], v[86:87], v[6:7], v[2:3]
	v_max_i32_e32 v6, 0, v16
	v_max_i32_e32 v7, 0, v32
	v_pk_fma_f32 v[4:5], v[88:89], v[6:7], v[4:5]
	v_max_i32_e32 v6, 0, v9
	v_max_i32_e32 v7, 0, v25
	v_pk_fma_f32 v[2:3], v[40:41], v[6:7], v[2:3]
	v_max_i32_e32 v6, 0, v17
	v_max_i32_e32 v7, 0, v33
	v_pk_fma_f32 v[4:5], v[36:37], v[6:7], v[4:5]
	v_not_b32_e32 v6, v2
	v_or_b32_e32 v7, 0x80000000, v2
	v_cmp_gt_i32_e32 vcc, 0, v2
	v_not_b32_e32 v2, v3
	s_nop 0
	v_cndmask_b32_e32 v179, v7, v6, vcc
	v_or_b32_e32 v6, 0x80000000, v3
	v_cmp_gt_i32_e32 vcc, 0, v3
	v_or_b32_e32 v3, 0x80000000, v4
	s_nop 0
	v_cndmask_b32_e32 v113, v6, v2, vcc
	v_not_b32_e32 v2, v4
	v_cmp_gt_i32_e32 vcc, 0, v4
	v_permlane32_swap_b32_e32 v179, v113
	s_nop 0
	v_cndmask_b32_e32 v142, v3, v2, vcc
	v_not_b32_e32 v2, v5
	v_or_b32_e32 v3, 0x80000000, v5
	v_cmp_gt_i32_e32 vcc, 0, v5
	s_nop 1
	v_cndmask_b32_e32 v94, v3, v2, vcc
	s_nop 1
	v_permlane32_swap_b32_e32 v142, v94

.LBB0_952:
	s_barrier
	ds_read_b128 v[2:5], v1 offset:16384
	ds_read_b128 v[18:21], v1 offset:20480
	ds_read_b128 v[96:99], v67 offset:16384
	ds_read_b128 v[228:231], v67 offset:20480
	ds_read_b128 v[232:235], v69 offset:16384
	ds_read_b128 v[236:239], v69 offset:20480
	ds_read_b128 v[240:243], v92 offset:16384
	ds_read_b128 v[244:247], v92 offset:20480
	s_cmp_lt_u32 s2, 18
	s_cbranch_scc1 .LBB0_954
	s_mov_b64 s[6:7], 0x12000
	v_lshl_add_u64 v[6:7], v[90:91], 0, s[6:7]
	s_add_i32 m0, s24, 0x2000
	s_nop 0
	global_load_lds_dwordx4 v[6:7], off
.LBB0_954:
	s_waitcnt lgkmcnt(5)
	v_mfma_f32_32x32x16_bf16 v[2:17], v[62:65], v[2:5], 0
	v_mfma_f32_32x32x16_bf16 v[18:33], v[62:65], v[18:21], 0
	v_mfma_f32_32x32x16_bf16 v[2:17], v[58:61], v[96:99], v[2:17]
	s_waitcnt lgkmcnt(4)
	v_mfma_f32_32x32x16_bf16 v[18:33], v[58:61], v[228:231], v[18:33]
	s_waitcnt lgkmcnt(3)
	v_mfma_f32_32x32x16_bf16 v[2:17], v[54:57], v[232:235], v[2:17]
	s_waitcnt lgkmcnt(2)
	v_mfma_f32_32x32x16_bf16 v[18:33], v[54:57], v[236:239], v[18:33]
	s_waitcnt lgkmcnt(1)
	v_mfma_f32_32x32x16_bf16 v[2:17], v[50:53], v[240:243], v[2:17]
	s_waitcnt lgkmcnt(0)
	v_mfma_f32_32x32x16_bf16 v[18:33], v[50:53], v[244:247], v[18:33]
	s_nop 9
	v_max_i32_e32 v100, 0, v2
	v_max_i32_e32 v98, 0, v10
	v_max_i32_e32 v2, 0, v3
	v_max_i32_e32 v10, 0, v11
	v_max_i32_e32 v101, 0, v18
	v_pk_fma_f32 v[96:97], v[74:75], v[100:101], 0 op_sel_hi:[1,1,0]
	v_max_i32_e32 v99, 0, v26
	v_max_i32_e32 v3, 0, v19
	v_pk_fma_f32 v[98:99], v[76:77], v[98:99], 0 op_sel_hi:[1,1,0]
	v_pk_fma_f32 v[2:3], v[46:47], v[2:3], v[96:97]
	v_max_i32_e32 v11, 0, v27
	v_max_i32_e32 v18, 0, v4
	v_max_i32_e32 v19, 0, v20
	v_pk_fma_f32 v[10:11], v[42:43], v[10:11], v[98:99]
	v_pk_fma_f32 v[2:3], v[78:79], v[18:19], v[2:3]
	v_max_i32_e32 v18, 0, v12
	v_max_i32_e32 v19, 0, v28
	v_max_i32_e32 v4, 0, v5
	v_max_i32_e32 v5, 0, v21
	v_pk_fma_f32 v[10:11], v[80:81], v[18:19], v[10:11]
	v_pk_fma_f32 v[2:3], v[48:49], v[4:5], v[2:3]
	v_max_i32_e32 v4, 0, v13
	v_max_i32_e32 v5, 0, v29
	v_pk_fma_f32 v[4:5], v[44:45], v[4:5], v[10:11]
	v_max_i32_e32 v10, 0, v6
	v_max_i32_e32 v11, 0, v22
	v_pk_fma_f32 v[2:3], v[82:83], v[10:11], v[2:3]
	v_max_i32_e32 v10, 0, v14
	v_max_i32_e32 v11, 0, v30
	v_max_i32_e32 v6, 0, v7
	v_max_i32_e32 v7, 0, v23
	v_pk_fma_f32 v[4:5], v[84:85], v[10:11], v[4:5]
	v_pk_fma_f32 v[2:3], v[38:39], v[6:7], v[2:3]
	v_max_i32_e32 v6, 0, v15
	v_max_i32_e32 v7, 0, v31
	v_pk_fma_f32 v[4:5], v[34:35], v[6:7], v[4:5]
	v_max_i32_e32 v6, 0, v8
	v_max_i32_e32 v7, 0, v24
	v_pk_fma_f32 v[2:3], v[86:87], v[6:7], v[2:3]
	v_max_i32_e32 v6, 0, v16
	v_max_i32_e32 v7, 0, v32
	v_pk_fma_f32 v[4:5], v[88:89], v[6:7], v[4:5]
	v_max_i32_e32 v6, 0, v9
	v_max_i32_e32 v7, 0, v25
	v_pk_fma_f32 v[2:3], v[40:41], v[6:7], v[2:3]
	v_max_i32_e32 v6, 0, v17
	v_max_i32_e32 v7, 0, v33
	v_pk_fma_f32 v[4:5], v[36:37], v[6:7], v[4:5]
	v_not_b32_e32 v6, v2
	v_or_b32_e32 v7, 0x80000000, v2
	v_cmp_gt_i32_e32 vcc, 0, v2
	v_not_b32_e32 v2, v3
	s_nop 0
	v_cndmask_b32_e32 v181, v7, v6, vcc
	v_or_b32_e32 v6, 0x80000000, v3
	v_cmp_gt_i32_e32 vcc, 0, v3
	v_or_b32_e32 v3, 0x80000000, v4
	s_nop 0
	v_cndmask_b32_e32 v115, v6, v2, vcc
	v_not_b32_e32 v2, v4
	v_cmp_gt_i32_e32 vcc, 0, v4
	v_permlane32_swap_b32_e32 v181, v115
	s_nop 0
	v_cndmask_b32_e32 v144, v3, v2, vcc
	v_not_b32_e32 v2, v5
	v_or_b32_e32 v3, 0x80000000, v5
	v_cmp_gt_i32_e32 vcc, 0, v5
	s_nop 1
	v_cndmask_b32_e32 v95, v3, v2, vcc
	s_nop 1
	v_permlane32_swap_b32_e32 v144, v95

.LBB0_978:
	s_barrier
	ds_read_b128 v[2:5], v1 offset:24576
	ds_read_b128 v[18:21], v1 offset:28672
	ds_read_b128 v[96:99], v67 offset:24576
	ds_read_b128 v[228:231], v67 offset:28672
	ds_read_b128 v[232:235], v69 offset:24576
	ds_read_b128 v[236:239], v69 offset:28672
	ds_read_b128 v[240:243], v92 offset:24576
	ds_read_b128 v[244:247], v92 offset:28672
	s_cmp_lt_u32 s2, 20
	s_cbranch_scc1 .LBB0_980
	s_mov_b64 s[4:5], 0x14000
	v_lshl_add_u64 v[6:7], v[90:91], 0, s[4:5]
	s_add_i32 m0, s24, 0x4000
	s_nop 0
	global_load_lds_dwordx4 v[6:7], off
.LBB0_980:
	s_waitcnt lgkmcnt(5)
	v_mfma_f32_32x32x16_bf16 v[2:17], v[62:65], v[2:5], 0
	v_mfma_f32_32x32x16_bf16 v[18:33], v[62:65], v[18:21], 0
	v_mfma_f32_32x32x16_bf16 v[2:17], v[58:61], v[96:99], v[2:17]
	s_waitcnt lgkmcnt(4)
	v_mfma_f32_32x32x16_bf16 v[18:33], v[58:61], v[228:231], v[18:33]
	s_waitcnt lgkmcnt(3)
	v_mfma_f32_32x32x16_bf16 v[2:17], v[54:57], v[232:235], v[2:17]
	s_waitcnt lgkmcnt(2)
	v_mfma_f32_32x32x16_bf16 v[18:33], v[54:57], v[236:239], v[18:33]
	s_waitcnt lgkmcnt(1)
	v_mfma_f32_32x32x16_bf16 v[2:17], v[50:53], v[240:243], v[2:17]
	s_waitcnt lgkmcnt(0)
	v_mfma_f32_32x32x16_bf16 v[18:33], v[50:53], v[244:247], v[18:33]
	s_nop 9
	v_max_i32_e32 v100, 0, v2
	v_max_i32_e32 v98, 0, v10
	v_max_i32_e32 v2, 0, v3
	v_max_i32_e32 v10, 0, v11
	v_max_i32_e32 v101, 0, v18
	v_pk_fma_f32 v[96:97], v[74:75], v[100:101], 0 op_sel_hi:[1,1,0]
	v_max_i32_e32 v99, 0, v26
	v_max_i32_e32 v3, 0, v19
	v_pk_fma_f32 v[98:99], v[76:77], v[98:99], 0 op_sel_hi:[1,1,0]
	v_pk_fma_f32 v[2:3], v[46:47], v[2:3], v[96:97]
	v_max_i32_e32 v11, 0, v27
	v_max_i32_e32 v18, 0, v4
	v_max_i32_e32 v19, 0, v20
	v_pk_fma_f32 v[10:11], v[42:43], v[10:11], v[98:99]
	v_pk_fma_f32 v[2:3], v[78:79], v[18:19], v[2:3]
	v_max_i32_e32 v18, 0, v12
	v_max_i32_e32 v19, 0, v28
	v_max_i32_e32 v4, 0, v5
	v_max_i32_e32 v5, 0, v21
	v_pk_fma_f32 v[10:11], v[80:81], v[18:19], v[10:11]
	v_pk_fma_f32 v[2:3], v[48:49], v[4:5], v[2:3]
	v_max_i32_e32 v4, 0, v13
	v_max_i32_e32 v5, 0, v29
	v_pk_fma_f32 v[4:5], v[44:45], v[4:5], v[10:11]
	v_max_i32_e32 v10, 0, v6
	v_max_i32_e32 v11, 0, v22
	v_pk_fma_f32 v[2:3], v[82:83], v[10:11], v[2:3]
	v_max_i32_e32 v10, 0, v14
	v_max_i32_e32 v11, 0, v30
	v_max_i32_e32 v6, 0, v7
	v_max_i32_e32 v7, 0, v23
	v_pk_fma_f32 v[4:5], v[84:85], v[10:11], v[4:5]
	v_pk_fma_f32 v[2:3], v[38:39], v[6:7], v[2:3]
	v_max_i32_e32 v6, 0, v15
	v_max_i32_e32 v7, 0, v31
	v_pk_fma_f32 v[4:5], v[34:35], v[6:7], v[4:5]
	v_max_i32_e32 v6, 0, v8
	v_max_i32_e32 v7, 0, v24
	v_pk_fma_f32 v[2:3], v[86:87], v[6:7], v[2:3]
	v_max_i32_e32 v6, 0, v16
	v_max_i32_e32 v7, 0, v32
	v_pk_fma_f32 v[4:5], v[88:89], v[6:7], v[4:5]
	v_max_i32_e32 v6, 0, v9
	v_max_i32_e32 v7, 0, v25
	v_pk_fma_f32 v[2:3], v[40:41], v[6:7], v[2:3]
	v_max_i32_e32 v6, 0, v17
	v_max_i32_e32 v7, 0, v33
	v_pk_fma_f32 v[4:5], v[36:37], v[6:7], v[4:5]
	v_not_b32_e32 v6, v2
	v_or_b32_e32 v7, 0x80000000, v2
	v_cmp_gt_i32_e32 vcc, 0, v2
	v_not_b32_e32 v2, v3
	s_nop 0
	v_cndmask_b32_e32 v183, v7, v6, vcc
	v_or_b32_e32 v6, 0x80000000, v3
	v_cmp_gt_i32_e32 vcc, 0, v3
	v_or_b32_e32 v3, 0x80000000, v4
	s_nop 0
	v_cndmask_b32_e32 v117, v6, v2, vcc
	v_not_b32_e32 v2, v4
	v_cmp_gt_i32_e32 vcc, 0, v4
	v_permlane32_swap_b32_e32 v183, v117
	s_nop 0
	v_cndmask_b32_e32 v146, v3, v2, vcc
	v_not_b32_e32 v2, v5
	v_or_b32_e32 v3, 0x80000000, v5
	v_cmp_gt_i32_e32 vcc, 0, v5
	s_nop 1
	v_cndmask_b32_e32 v96, v3, v2, vcc
	s_nop 1
	v_permlane32_swap_b32_e32 v146, v96

.LBB0_1004:
	s_barrier
	ds_read_b128 v[2:5], v1 offset:32768
	ds_read_b128 v[18:21], v1 offset:36864
	ds_read_b128 v[98:101], v67 offset:32768
	ds_read_b128 v[228:231], v67 offset:36864
	ds_read_b128 v[232:235], v69 offset:32768
	ds_read_b128 v[236:239], v69 offset:36864
	ds_read_b128 v[240:243], v92 offset:32768
	ds_read_b128 v[244:247], v92 offset:36864
	s_cmp_lt_u32 s2, 22
	s_cbranch_scc1 .LBB0_1006
	s_mov_b64 s[4:5], 0x16000
	v_lshl_add_u64 v[6:7], v[90:91], 0, s[4:5]
	s_add_i32 m0, s24, 0x6000
	s_nop 0
	global_load_lds_dwordx4 v[6:7], off
.LBB0_1006:
	s_waitcnt lgkmcnt(5)
	v_mfma_f32_32x32x16_bf16 v[2:17], v[62:65], v[2:5], 0
	v_mfma_f32_32x32x16_bf16 v[18:33], v[62:65], v[18:21], 0
	v_mfma_f32_32x32x16_bf16 v[2:17], v[58:61], v[98:101], v[2:17]
	s_waitcnt lgkmcnt(4)
	v_mfma_f32_32x32x16_bf16 v[18:33], v[58:61], v[228:231], v[18:33]
	s_waitcnt lgkmcnt(3)
	v_mfma_f32_32x32x16_bf16 v[2:17], v[54:57], v[232:235], v[2:17]
	s_waitcnt lgkmcnt(2)
	v_mfma_f32_32x32x16_bf16 v[18:33], v[54:57], v[236:239], v[18:33]
	s_waitcnt lgkmcnt(1)
	v_mfma_f32_32x32x16_bf16 v[2:17], v[50:53], v[240:243], v[2:17]
	s_waitcnt lgkmcnt(0)
	v_mfma_f32_32x32x16_bf16 v[18:33], v[50:53], v[244:247], v[18:33]
	s_nop 9
	v_max_i32_e32 v102, 0, v2
	v_max_i32_e32 v100, 0, v10
	v_max_i32_e32 v2, 0, v3
	v_max_i32_e32 v10, 0, v11
	v_max_i32_e32 v103, 0, v18
	v_pk_fma_f32 v[98:99], v[74:75], v[102:103], 0 op_sel_hi:[1,1,0]
	v_max_i32_e32 v101, 0, v26
	v_max_i32_e32 v3, 0, v19
	v_pk_fma_f32 v[100:101], v[76:77], v[100:101], 0 op_sel_hi:[1,1,0]
	v_pk_fma_f32 v[2:3], v[46:47], v[2:3], v[98:99]
	v_max_i32_e32 v11, 0, v27
	v_max_i32_e32 v18, 0, v4
	v_max_i32_e32 v19, 0, v20
	v_pk_fma_f32 v[10:11], v[42:43], v[10:11], v[100:101]
	v_pk_fma_f32 v[2:3], v[78:79], v[18:19], v[2:3]
	v_max_i32_e32 v18, 0, v12
	v_max_i32_e32 v19, 0, v28
	v_max_i32_e32 v4, 0, v5
	v_max_i32_e32 v5, 0, v21
	v_pk_fma_f32 v[10:11], v[80:81], v[18:19], v[10:11]
	v_pk_fma_f32 v[2:3], v[48:49], v[4:5], v[2:3]
	v_max_i32_e32 v4, 0, v13
	v_max_i32_e32 v5, 0, v29
	v_pk_fma_f32 v[4:5], v[44:45], v[4:5], v[10:11]
	v_max_i32_e32 v10, 0, v6
	v_max_i32_e32 v11, 0, v22
	v_pk_fma_f32 v[2:3], v[82:83], v[10:11], v[2:3]
	v_max_i32_e32 v10, 0, v14
	v_max_i32_e32 v11, 0, v30
	v_max_i32_e32 v6, 0, v7
	v_max_i32_e32 v7, 0, v23
	v_pk_fma_f32 v[4:5], v[84:85], v[10:11], v[4:5]
	v_pk_fma_f32 v[2:3], v[38:39], v[6:7], v[2:3]
	v_max_i32_e32 v6, 0, v15
	v_max_i32_e32 v7, 0, v31
	v_pk_fma_f32 v[4:5], v[34:35], v[6:7], v[4:5]
	v_max_i32_e32 v6, 0, v8
	v_max_i32_e32 v7, 0, v24
	v_pk_fma_f32 v[2:3], v[86:87], v[6:7], v[2:3]
	v_max_i32_e32 v6, 0, v16
	v_max_i32_e32 v7, 0, v32
	v_pk_fma_f32 v[4:5], v[88:89], v[6:7], v[4:5]
	v_max_i32_e32 v6, 0, v9
	v_max_i32_e32 v7, 0, v25
	v_pk_fma_f32 v[2:3], v[40:41], v[6:7], v[2:3]
	v_max_i32_e32 v6, 0, v17
	v_max_i32_e32 v7, 0, v33
	v_pk_fma_f32 v[4:5], v[36:37], v[6:7], v[4:5]
	v_not_b32_e32 v6, v2
	v_or_b32_e32 v7, 0x80000000, v2
	v_cmp_gt_i32_e32 vcc, 0, v2
	v_not_b32_e32 v2, v3
	s_nop 0
	v_cndmask_b32_e32 v185, v7, v6, vcc
	v_or_b32_e32 v6, 0x80000000, v3
	v_cmp_gt_i32_e32 vcc, 0, v3
	v_or_b32_e32 v3, 0x80000000, v4
	s_nop 0
	v_cndmask_b32_e32 v119, v6, v2, vcc
	v_not_b32_e32 v2, v4
	v_cmp_gt_i32_e32 vcc, 0, v4
	v_permlane32_swap_b32_e32 v185, v119
	s_nop 0
	v_cndmask_b32_e32 v148, v3, v2, vcc
	v_not_b32_e32 v2, v5
	v_or_b32_e32 v3, 0x80000000, v5
	v_cmp_gt_i32_e32 vcc, 0, v5
	s_nop 1
	v_cndmask_b32_e32 v97, v3, v2, vcc
	s_nop 1
	v_permlane32_swap_b32_e32 v148, v97

.LBB0_1030:
	s_barrier
	ds_read_b128 v[2:5], v1 offset:40960
	ds_read_b128 v[18:21], v1 offset:45056
	ds_read_b128 v[98:101], v67 offset:40960
	ds_read_b128 v[228:231], v67 offset:45056
	ds_read_b128 v[232:235], v69 offset:40960
	ds_read_b128 v[236:239], v69 offset:45056
	ds_read_b128 v[240:243], v92 offset:40960
	ds_read_b128 v[244:247], v92 offset:45056
	s_cmp_lt_u32 s2, 24
	s_cbranch_scc1 .LBB0_1032
	s_mov_b64 s[4:5], 0x18000
	v_lshl_add_u64 v[6:7], v[90:91], 0, s[4:5]
	s_add_i32 m0, s24, 0x8000
	s_nop 0
	global_load_lds_dwordx4 v[6:7], off
.LBB0_1032:
	s_waitcnt lgkmcnt(5)
	v_mfma_f32_32x32x16_bf16 v[2:17], v[62:65], v[2:5], 0
	v_mfma_f32_32x32x16_bf16 v[18:33], v[62:65], v[18:21], 0
	v_mfma_f32_32x32x16_bf16 v[2:17], v[58:61], v[98:101], v[2:17]
	s_waitcnt lgkmcnt(4)
	v_mfma_f32_32x32x16_bf16 v[18:33], v[58:61], v[228:231], v[18:33]
	s_waitcnt lgkmcnt(3)
	v_mfma_f32_32x32x16_bf16 v[2:17], v[54:57], v[232:235], v[2:17]
	s_waitcnt lgkmcnt(2)
	v_mfma_f32_32x32x16_bf16 v[18:33], v[54:57], v[236:239], v[18:33]
	s_waitcnt lgkmcnt(1)
	v_mfma_f32_32x32x16_bf16 v[2:17], v[50:53], v[240:243], v[2:17]
	s_waitcnt lgkmcnt(0)
	v_mfma_f32_32x32x16_bf16 v[18:33], v[50:53], v[244:247], v[18:33]
	s_nop 9
	v_max_i32_e32 v102, 0, v2
	v_max_i32_e32 v100, 0, v10
	v_max_i32_e32 v2, 0, v3
	v_max_i32_e32 v10, 0, v11
	v_max_i32_e32 v103, 0, v18
	v_pk_fma_f32 v[98:99], v[74:75], v[102:103], 0 op_sel_hi:[1,1,0]
	v_max_i32_e32 v101, 0, v26
	v_max_i32_e32 v3, 0, v19
	v_pk_fma_f32 v[100:101], v[76:77], v[100:101], 0 op_sel_hi:[1,1,0]
	v_pk_fma_f32 v[2:3], v[46:47], v[2:3], v[98:99]
	v_max_i32_e32 v11, 0, v27
	v_max_i32_e32 v18, 0, v4
	v_max_i32_e32 v19, 0, v20
	v_pk_fma_f32 v[10:11], v[42:43], v[10:11], v[100:101]
	v_pk_fma_f32 v[2:3], v[78:79], v[18:19], v[2:3]
	v_max_i32_e32 v18, 0, v12
	v_max_i32_e32 v19, 0, v28
	v_max_i32_e32 v4, 0, v5
	v_max_i32_e32 v5, 0, v21
	v_pk_fma_f32 v[10:11], v[80:81], v[18:19], v[10:11]
	v_pk_fma_f32 v[2:3], v[48:49], v[4:5], v[2:3]
	v_max_i32_e32 v4, 0, v13
	v_max_i32_e32 v5, 0, v29
	v_pk_fma_f32 v[4:5], v[44:45], v[4:5], v[10:11]
	v_max_i32_e32 v10, 0, v6
	v_max_i32_e32 v11, 0, v22
	v_pk_fma_f32 v[2:3], v[82:83], v[10:11], v[2:3]
	v_max_i32_e32 v10, 0, v14
	v_max_i32_e32 v11, 0, v30
	v_max_i32_e32 v6, 0, v7
	v_max_i32_e32 v7, 0, v23
	v_pk_fma_f32 v[4:5], v[84:85], v[10:11], v[4:5]
	v_pk_fma_f32 v[2:3], v[38:39], v[6:7], v[2:3]
	v_max_i32_e32 v6, 0, v15
	v_max_i32_e32 v7, 0, v31
	v_pk_fma_f32 v[4:5], v[34:35], v[6:7], v[4:5]
	v_max_i32_e32 v6, 0, v8
	v_max_i32_e32 v7, 0, v24
	v_pk_fma_f32 v[2:3], v[86:87], v[6:7], v[2:3]
	v_max_i32_e32 v6, 0, v16
	v_max_i32_e32 v7, 0, v32
	v_pk_fma_f32 v[4:5], v[88:89], v[6:7], v[4:5]
	v_max_i32_e32 v6, 0, v9
	v_max_i32_e32 v7, 0, v25
	v_pk_fma_f32 v[2:3], v[40:41], v[6:7], v[2:3]
	v_max_i32_e32 v6, 0, v17
	v_max_i32_e32 v7, 0, v33
	v_pk_fma_f32 v[4:5], v[36:37], v[6:7], v[4:5]
	v_not_b32_e32 v6, v2
	v_or_b32_e32 v7, 0x80000000, v2
	v_cmp_gt_i32_e32 vcc, 0, v2
	v_not_b32_e32 v2, v3
	s_nop 0
	v_cndmask_b32_e32 v187, v7, v6, vcc
	v_or_b32_e32 v6, 0x80000000, v3
	v_cmp_gt_i32_e32 vcc, 0, v3
	v_or_b32_e32 v3, 0x80000000, v4
	s_nop 0
	v_cndmask_b32_e32 v121, v6, v2, vcc
	v_not_b32_e32 v2, v4
	v_cmp_gt_i32_e32 vcc, 0, v4
	v_permlane32_swap_b32_e32 v187, v121
	s_nop 0
	v_cndmask_b32_e32 v150, v3, v2, vcc
	v_not_b32_e32 v2, v5
	v_or_b32_e32 v3, 0x80000000, v5
	v_cmp_gt_i32_e32 vcc, 0, v5
	s_nop 1
	v_cndmask_b32_e32 v98, v3, v2, vcc
	s_nop 1
	v_permlane32_swap_b32_e32 v150, v98

.LBB0_1056:
	s_barrier
	ds_read_b128 v[2:5], v1 offset:49152
	ds_read_b128 v[18:21], v1 offset:53248
	ds_read_b128 v[100:103], v67 offset:49152
	ds_read_b128 v[228:231], v67 offset:53248
	ds_read_b128 v[232:235], v69 offset:49152
	ds_read_b128 v[236:239], v69 offset:53248
	ds_read_b128 v[240:243], v92 offset:49152
	ds_read_b128 v[244:247], v92 offset:53248
	s_cmp_lt_u32 s2, 26
	s_cbranch_scc1 .LBB0_1058
	s_mov_b64 s[4:5], 0x1a000
	v_lshl_add_u64 v[6:7], v[90:91], 0, s[4:5]
	s_add_i32 m0, s24, 0xa000
	s_nop 0
	global_load_lds_dwordx4 v[6:7], off
.LBB0_1058:
	s_waitcnt lgkmcnt(5)
	v_mfma_f32_32x32x16_bf16 v[2:17], v[62:65], v[2:5], 0
	v_mfma_f32_32x32x16_bf16 v[18:33], v[62:65], v[18:21], 0
	v_mfma_f32_32x32x16_bf16 v[2:17], v[58:61], v[100:103], v[2:17]
	s_waitcnt lgkmcnt(4)
	v_mfma_f32_32x32x16_bf16 v[18:33], v[58:61], v[228:231], v[18:33]
	s_waitcnt lgkmcnt(3)
	v_mfma_f32_32x32x16_bf16 v[2:17], v[54:57], v[232:235], v[2:17]
	s_waitcnt lgkmcnt(2)
	v_mfma_f32_32x32x16_bf16 v[18:33], v[54:57], v[236:239], v[18:33]
	s_waitcnt lgkmcnt(1)
	v_mfma_f32_32x32x16_bf16 v[2:17], v[50:53], v[240:243], v[2:17]
	s_waitcnt lgkmcnt(0)
	v_mfma_f32_32x32x16_bf16 v[18:33], v[50:53], v[244:247], v[18:33]
	s_nop 9
	v_max_i32_e32 v104, 0, v2
	v_max_i32_e32 v102, 0, v10
	v_max_i32_e32 v2, 0, v3
	v_max_i32_e32 v10, 0, v11
	v_max_i32_e32 v105, 0, v18
	v_pk_fma_f32 v[100:101], v[74:75], v[104:105], 0 op_sel_hi:[1,1,0]
	v_max_i32_e32 v103, 0, v26
	v_max_i32_e32 v3, 0, v19
	v_pk_fma_f32 v[102:103], v[76:77], v[102:103], 0 op_sel_hi:[1,1,0]
	v_pk_fma_f32 v[2:3], v[46:47], v[2:3], v[100:101]
	v_max_i32_e32 v11, 0, v27
	v_max_i32_e32 v18, 0, v4
	v_max_i32_e32 v19, 0, v20
	v_pk_fma_f32 v[10:11], v[42:43], v[10:11], v[102:103]
	v_pk_fma_f32 v[2:3], v[78:79], v[18:19], v[2:3]
	v_max_i32_e32 v18, 0, v12
	v_max_i32_e32 v19, 0, v28
	v_max_i32_e32 v4, 0, v5
	v_max_i32_e32 v5, 0, v21
	v_pk_fma_f32 v[10:11], v[80:81], v[18:19], v[10:11]
	v_pk_fma_f32 v[2:3], v[48:49], v[4:5], v[2:3]
	v_max_i32_e32 v4, 0, v13
	v_max_i32_e32 v5, 0, v29
	v_pk_fma_f32 v[4:5], v[44:45], v[4:5], v[10:11]
	v_max_i32_e32 v10, 0, v6
	v_max_i32_e32 v11, 0, v22
	v_pk_fma_f32 v[2:3], v[82:83], v[10:11], v[2:3]
	v_max_i32_e32 v10, 0, v14
	v_max_i32_e32 v11, 0, v30
	v_max_i32_e32 v6, 0, v7
	v_max_i32_e32 v7, 0, v23
	v_pk_fma_f32 v[4:5], v[84:85], v[10:11], v[4:5]
	v_pk_fma_f32 v[2:3], v[38:39], v[6:7], v[2:3]
	v_max_i32_e32 v6, 0, v15
	v_max_i32_e32 v7, 0, v31
	v_pk_fma_f32 v[4:5], v[34:35], v[6:7], v[4:5]
	v_max_i32_e32 v6, 0, v8
	v_max_i32_e32 v7, 0, v24
	v_pk_fma_f32 v[2:3], v[86:87], v[6:7], v[2:3]
	v_max_i32_e32 v6, 0, v16
	v_max_i32_e32 v7, 0, v32
	v_pk_fma_f32 v[4:5], v[88:89], v[6:7], v[4:5]
	v_max_i32_e32 v6, 0, v9
	v_max_i32_e32 v7, 0, v25
	v_pk_fma_f32 v[2:3], v[40:41], v[6:7], v[2:3]
	v_max_i32_e32 v6, 0, v17
	v_max_i32_e32 v7, 0, v33
	v_pk_fma_f32 v[4:5], v[36:37], v[6:7], v[4:5]
	v_not_b32_e32 v6, v2
	v_or_b32_e32 v7, 0x80000000, v2
	v_cmp_gt_i32_e32 vcc, 0, v2
	v_not_b32_e32 v2, v3
	s_nop 0
	v_cndmask_b32_e32 v189, v7, v6, vcc
	v_or_b32_e32 v6, 0x80000000, v3
	v_cmp_gt_i32_e32 vcc, 0, v3
	v_or_b32_e32 v3, 0x80000000, v4
	s_nop 0
	v_cndmask_b32_e32 v123, v6, v2, vcc
	v_not_b32_e32 v2, v4
	v_cmp_gt_i32_e32 vcc, 0, v4
	v_permlane32_swap_b32_e32 v189, v123
	s_nop 0
	v_cndmask_b32_e32 v152, v3, v2, vcc
	v_not_b32_e32 v2, v5
	v_or_b32_e32 v3, 0x80000000, v5
	v_cmp_gt_i32_e32 vcc, 0, v5
	s_nop 1
	v_cndmask_b32_e32 v99, v3, v2, vcc
	s_nop 1
	v_permlane32_swap_b32_e32 v152, v99

.LBB0_1082:
	s_barrier
	ds_read_b128 v[2:5], v1 offset:57344
	ds_read_b128 v[18:21], v1 offset:61440
	ds_read_b128 v[100:103], v67 offset:57344
	ds_read_b128 v[228:231], v67 offset:61440
	ds_read_b128 v[232:235], v69 offset:57344
	ds_read_b128 v[236:239], v69 offset:61440
	ds_read_b128 v[240:243], v92 offset:57344
	ds_read_b128 v[244:247], v92 offset:61440
	s_cmp_lt_u32 s2, 28
	s_cbranch_scc1 .LBB0_1084
	s_mov_b64 s[4:5], 0x1c000
	v_lshl_add_u64 v[6:7], v[90:91], 0, s[4:5]
	s_add_i32 m0, s24, 0xc000
	s_nop 0
	global_load_lds_dwordx4 v[6:7], off
.LBB0_1084:
	s_waitcnt lgkmcnt(5)
	v_mfma_f32_32x32x16_bf16 v[2:17], v[62:65], v[2:5], 0
	v_mfma_f32_32x32x16_bf16 v[18:33], v[62:65], v[18:21], 0
	v_mfma_f32_32x32x16_bf16 v[2:17], v[58:61], v[100:103], v[2:17]
	s_waitcnt lgkmcnt(4)
	v_mfma_f32_32x32x16_bf16 v[18:33], v[58:61], v[228:231], v[18:33]
	s_waitcnt lgkmcnt(3)
	v_mfma_f32_32x32x16_bf16 v[2:17], v[54:57], v[232:235], v[2:17]
	s_waitcnt lgkmcnt(2)
	v_mfma_f32_32x32x16_bf16 v[18:33], v[54:57], v[236:239], v[18:33]
	s_waitcnt lgkmcnt(1)
	v_mfma_f32_32x32x16_bf16 v[2:17], v[50:53], v[240:243], v[2:17]
	s_waitcnt lgkmcnt(0)
	v_mfma_f32_32x32x16_bf16 v[18:33], v[50:53], v[244:247], v[18:33]
	s_nop 9
	v_max_i32_e32 v104, 0, v2
	v_max_i32_e32 v102, 0, v10
	v_max_i32_e32 v2, 0, v3
	v_max_i32_e32 v10, 0, v11
	v_max_i32_e32 v105, 0, v18
	v_pk_fma_f32 v[100:101], v[74:75], v[104:105], 0 op_sel_hi:[1,1,0]
	v_max_i32_e32 v103, 0, v26
	v_max_i32_e32 v3, 0, v19
	v_pk_fma_f32 v[102:103], v[76:77], v[102:103], 0 op_sel_hi:[1,1,0]
	v_pk_fma_f32 v[2:3], v[46:47], v[2:3], v[100:101]
	v_max_i32_e32 v11, 0, v27
	v_max_i32_e32 v18, 0, v4
	v_max_i32_e32 v19, 0, v20
	v_pk_fma_f32 v[10:11], v[42:43], v[10:11], v[102:103]
	v_pk_fma_f32 v[2:3], v[78:79], v[18:19], v[2:3]
	v_max_i32_e32 v18, 0, v12
	v_max_i32_e32 v19, 0, v28
	v_max_i32_e32 v4, 0, v5
	v_max_i32_e32 v5, 0, v21
	v_pk_fma_f32 v[10:11], v[80:81], v[18:19], v[10:11]
	v_pk_fma_f32 v[2:3], v[48:49], v[4:5], v[2:3]
	v_max_i32_e32 v4, 0, v13
	v_max_i32_e32 v5, 0, v29
	v_pk_fma_f32 v[4:5], v[44:45], v[4:5], v[10:11]
	v_max_i32_e32 v10, 0, v6
	v_max_i32_e32 v11, 0, v22
	v_pk_fma_f32 v[2:3], v[82:83], v[10:11], v[2:3]
	v_max_i32_e32 v10, 0, v14
	v_max_i32_e32 v11, 0, v30
	v_max_i32_e32 v6, 0, v7
	v_max_i32_e32 v7, 0, v23
	v_pk_fma_f32 v[4:5], v[84:85], v[10:11], v[4:5]
	v_pk_fma_f32 v[2:3], v[38:39], v[6:7], v[2:3]
	v_max_i32_e32 v6, 0, v15
	v_max_i32_e32 v7, 0, v31
	v_pk_fma_f32 v[4:5], v[34:35], v[6:7], v[4:5]
	v_max_i32_e32 v6, 0, v8
	v_max_i32_e32 v7, 0, v24
	v_pk_fma_f32 v[2:3], v[86:87], v[6:7], v[2:3]
	v_max_i32_e32 v6, 0, v16
	v_max_i32_e32 v7, 0, v32
	v_pk_fma_f32 v[4:5], v[88:89], v[6:7], v[4:5]
	v_max_i32_e32 v6, 0, v9
	v_max_i32_e32 v7, 0, v25
	v_pk_fma_f32 v[2:3], v[40:41], v[6:7], v[2:3]
	v_max_i32_e32 v6, 0, v17
	v_max_i32_e32 v7, 0, v33
	v_pk_fma_f32 v[4:5], v[36:37], v[6:7], v[4:5]
	v_not_b32_e32 v6, v2
	v_or_b32_e32 v7, 0x80000000, v2
	v_cmp_gt_i32_e32 vcc, 0, v2
	v_not_b32_e32 v2, v3
	s_nop 0
	v_cndmask_b32_e32 v190, v7, v6, vcc
	v_or_b32_e32 v6, 0x80000000, v3
	v_cmp_gt_i32_e32 vcc, 0, v3
	v_or_b32_e32 v3, 0x80000000, v4
	s_nop 0
	v_cndmask_b32_e32 v124, v6, v2, vcc
	v_not_b32_e32 v2, v4
	v_cmp_gt_i32_e32 vcc, 0, v4
	v_permlane32_swap_b32_e32 v190, v124
	s_nop 0
	v_cndmask_b32_e32 v153, v3, v2, vcc
	v_not_b32_e32 v2, v5
	v_or_b32_e32 v3, 0x80000000, v5
	v_cmp_gt_i32_e32 vcc, 0, v5
	s_nop 1
	v_cndmask_b32_e32 v100, v3, v2, vcc
	s_nop 1
	v_permlane32_swap_b32_e32 v153, v100

.LBB0_1108:
	s_barrier
	ds_read_b128 v[2:5], v1
	ds_read_b128 v[18:21], v1 offset:4096
	ds_read_b128 v[102:105], v67
	ds_read_b128 v[228:231], v67 offset:4096
	ds_read_b128 v[232:235], v69
	ds_read_b128 v[236:239], v69 offset:4096
	ds_read_b128 v[240:243], v92
	ds_read_b128 v[244:247], v92 offset:4096
	s_cmp_lt_u32 s2, 30
	s_cbranch_scc1 .LBB0_1110
	s_mov_b64 s[4:5], 0x1e000
	v_lshl_add_u64 v[6:7], v[90:91], 0, s[4:5]
	s_add_i32 m0, s24, 0xe000
	s_nop 0
	global_load_lds_dwordx4 v[6:7], off
.LBB0_1110:
	s_waitcnt lgkmcnt(5)
	v_mfma_f32_32x32x16_bf16 v[2:17], v[62:65], v[2:5], 0
	v_mfma_f32_32x32x16_bf16 v[18:33], v[62:65], v[18:21], 0
	v_mfma_f32_32x32x16_bf16 v[2:17], v[58:61], v[102:105], v[2:17]
	s_waitcnt lgkmcnt(4)
	v_mfma_f32_32x32x16_bf16 v[18:33], v[58:61], v[228:231], v[18:33]
	s_waitcnt lgkmcnt(3)
	v_mfma_f32_32x32x16_bf16 v[2:17], v[54:57], v[232:235], v[2:17]
	s_waitcnt lgkmcnt(2)
	v_mfma_f32_32x32x16_bf16 v[18:33], v[54:57], v[236:239], v[18:33]
	s_waitcnt lgkmcnt(1)
	v_mfma_f32_32x32x16_bf16 v[2:17], v[50:53], v[240:243], v[2:17]
	s_waitcnt lgkmcnt(0)
	v_mfma_f32_32x32x16_bf16 v[18:33], v[50:53], v[244:247], v[18:33]
	s_nop 9
	v_max_i32_e32 v106, 0, v2
	v_max_i32_e32 v104, 0, v10
	v_max_i32_e32 v2, 0, v3
	v_max_i32_e32 v10, 0, v11
	v_max_i32_e32 v107, 0, v18
	v_pk_fma_f32 v[102:103], v[74:75], v[106:107], 0 op_sel_hi:[1,1,0]
	v_max_i32_e32 v105, 0, v26
	v_max_i32_e32 v3, 0, v19
	v_pk_fma_f32 v[104:105], v[76:77], v[104:105], 0 op_sel_hi:[1,1,0]
	v_pk_fma_f32 v[2:3], v[46:47], v[2:3], v[102:103]
	v_max_i32_e32 v11, 0, v27
	v_max_i32_e32 v18, 0, v4
	v_max_i32_e32 v19, 0, v20
	v_pk_fma_f32 v[10:11], v[42:43], v[10:11], v[104:105]
	v_pk_fma_f32 v[2:3], v[78:79], v[18:19], v[2:3]
	v_max_i32_e32 v18, 0, v12
	v_max_i32_e32 v19, 0, v28
	v_max_i32_e32 v4, 0, v5
	v_max_i32_e32 v5, 0, v21
	v_pk_fma_f32 v[10:11], v[80:81], v[18:19], v[10:11]
	v_pk_fma_f32 v[2:3], v[48:49], v[4:5], v[2:3]
	v_max_i32_e32 v4, 0, v13
	v_max_i32_e32 v5, 0, v29
	v_pk_fma_f32 v[4:5], v[44:45], v[4:5], v[10:11]
	v_max_i32_e32 v10, 0, v6
	v_max_i32_e32 v11, 0, v22
	v_pk_fma_f32 v[2:3], v[82:83], v[10:11], v[2:3]
	v_max_i32_e32 v10, 0, v14
	v_max_i32_e32 v11, 0, v30
	v_max_i32_e32 v6, 0, v7
	v_max_i32_e32 v7, 0, v23
	v_pk_fma_f32 v[4:5], v[84:85], v[10:11], v[4:5]
	v_pk_fma_f32 v[2:3], v[38:39], v[6:7], v[2:3]
	v_max_i32_e32 v6, 0, v15
	v_max_i32_e32 v7, 0, v31
	v_pk_fma_f32 v[4:5], v[34:35], v[6:7], v[4:5]
	v_max_i32_e32 v6, 0, v8
	v_max_i32_e32 v7, 0, v24
	v_pk_fma_f32 v[2:3], v[86:87], v[6:7], v[2:3]
	v_max_i32_e32 v6, 0, v16
	v_max_i32_e32 v7, 0, v32
	v_pk_fma_f32 v[4:5], v[88:89], v[6:7], v[4:5]
	v_max_i32_e32 v6, 0, v9
	v_max_i32_e32 v7, 0, v25
	v_pk_fma_f32 v[2:3], v[40:41], v[6:7], v[2:3]
	v_max_i32_e32 v6, 0, v17
	v_max_i32_e32 v7, 0, v33
	v_pk_fma_f32 v[4:5], v[36:37], v[6:7], v[4:5]
	v_not_b32_e32 v6, v2
	v_or_b32_e32 v7, 0x80000000, v2
	v_cmp_gt_i32_e32 vcc, 0, v2
	v_not_b32_e32 v2, v3
	s_nop 0
	v_cndmask_b32_e32 v191, v7, v6, vcc
	v_or_b32_e32 v6, 0x80000000, v3
	v_cmp_gt_i32_e32 vcc, 0, v3
	v_or_b32_e32 v3, 0x80000000, v4
	s_nop 0
	v_cndmask_b32_e32 v125, v6, v2, vcc
	v_not_b32_e32 v2, v4
	v_cmp_gt_i32_e32 vcc, 0, v4
	v_permlane32_swap_b32_e32 v191, v125
	s_nop 0
	v_cndmask_b32_e32 v154, v3, v2, vcc
	v_not_b32_e32 v2, v5
	v_or_b32_e32 v3, 0x80000000, v5
	v_cmp_gt_i32_e32 vcc, 0, v5
	s_nop 1
	v_cndmask_b32_e32 v101, v3, v2, vcc
	s_nop 1
	v_permlane32_swap_b32_e32 v154, v101

.LBB0_1134:
	s_barrier
	ds_read_b128 v[2:5], v1 offset:8192
	ds_read_b128 v[18:21], v1 offset:12288
	ds_read_b128 v[102:105], v67 offset:8192
	ds_read_b128 v[228:231], v67 offset:12288
	ds_read_b128 v[232:235], v69 offset:8192
	ds_read_b128 v[236:239], v69 offset:12288
	ds_read_b128 v[240:243], v92 offset:8192
	ds_read_b128 v[244:247], v92 offset:12288
	s_cmp_lt_u32 s2, 32
	s_cbranch_scc1 .LBB0_1136
	s_mov_b64 s[4:5], 0x20000
	v_lshl_add_u64 v[6:7], v[90:91], 0, s[4:5]
	s_mov_b32 m0, s24
	s_nop 0
	global_load_lds_dwordx4 v[6:7], off
.LBB0_1136:
	s_waitcnt lgkmcnt(5)
	v_mfma_f32_32x32x16_bf16 v[2:17], v[62:65], v[2:5], 0
	v_mfma_f32_32x32x16_bf16 v[18:33], v[62:65], v[18:21], 0
	v_mfma_f32_32x32x16_bf16 v[2:17], v[58:61], v[102:105], v[2:17]
	s_waitcnt lgkmcnt(4)
	v_mfma_f32_32x32x16_bf16 v[18:33], v[58:61], v[228:231], v[18:33]
	s_waitcnt lgkmcnt(3)
	v_mfma_f32_32x32x16_bf16 v[2:17], v[54:57], v[232:235], v[2:17]
	s_waitcnt lgkmcnt(2)
	v_mfma_f32_32x32x16_bf16 v[18:33], v[54:57], v[236:239], v[18:33]
	s_waitcnt lgkmcnt(1)
	v_mfma_f32_32x32x16_bf16 v[2:17], v[50:53], v[240:243], v[2:17]
	s_waitcnt lgkmcnt(0)
	v_mfma_f32_32x32x16_bf16 v[18:33], v[50:53], v[244:247], v[18:33]
	s_nop 9
	v_max_i32_e32 v106, 0, v2
	v_max_i32_e32 v104, 0, v10
	v_max_i32_e32 v2, 0, v3
	v_max_i32_e32 v10, 0, v11
	v_max_i32_e32 v107, 0, v18
	v_pk_fma_f32 v[102:103], v[74:75], v[106:107], 0 op_sel_hi:[1,1,0]
	v_max_i32_e32 v105, 0, v26
	v_max_i32_e32 v3, 0, v19
	v_pk_fma_f32 v[104:105], v[76:77], v[104:105], 0 op_sel_hi:[1,1,0]
	v_pk_fma_f32 v[2:3], v[46:47], v[2:3], v[102:103]
	v_max_i32_e32 v11, 0, v27
	v_max_i32_e32 v18, 0, v4
	v_max_i32_e32 v19, 0, v20
	v_pk_fma_f32 v[10:11], v[42:43], v[10:11], v[104:105]
	v_pk_fma_f32 v[2:3], v[78:79], v[18:19], v[2:3]
	v_max_i32_e32 v18, 0, v12
	v_max_i32_e32 v19, 0, v28
	v_max_i32_e32 v4, 0, v5
	v_max_i32_e32 v5, 0, v21
	v_pk_fma_f32 v[10:11], v[80:81], v[18:19], v[10:11]
	v_pk_fma_f32 v[2:3], v[48:49], v[4:5], v[2:3]
	v_max_i32_e32 v4, 0, v13
	v_max_i32_e32 v5, 0, v29
	v_pk_fma_f32 v[4:5], v[44:45], v[4:5], v[10:11]
	v_max_i32_e32 v10, 0, v6
	v_max_i32_e32 v11, 0, v22
	v_pk_fma_f32 v[2:3], v[82:83], v[10:11], v[2:3]
	v_max_i32_e32 v10, 0, v14
	v_max_i32_e32 v11, 0, v30
	v_max_i32_e32 v6, 0, v7
	v_max_i32_e32 v7, 0, v23
	v_pk_fma_f32 v[4:5], v[84:85], v[10:11], v[4:5]
	v_pk_fma_f32 v[2:3], v[38:39], v[6:7], v[2:3]
	v_max_i32_e32 v6, 0, v15
	v_max_i32_e32 v7, 0, v31
	v_pk_fma_f32 v[4:5], v[34:35], v[6:7], v[4:5]
	v_max_i32_e32 v6, 0, v8
	v_max_i32_e32 v7, 0, v24
	v_pk_fma_f32 v[2:3], v[86:87], v[6:7], v[2:3]
	v_max_i32_e32 v6, 0, v16
	v_max_i32_e32 v7, 0, v32
	v_pk_fma_f32 v[4:5], v[88:89], v[6:7], v[4:5]
	v_max_i32_e32 v6, 0, v9
	v_max_i32_e32 v7, 0, v25
	v_pk_fma_f32 v[2:3], v[40:41], v[6:7], v[2:3]
	v_max_i32_e32 v6, 0, v17
	v_max_i32_e32 v7, 0, v33
	v_pk_fma_f32 v[4:5], v[36:37], v[6:7], v[4:5]
	v_not_b32_e32 v6, v2
	v_or_b32_e32 v7, 0x80000000, v2
	v_cmp_gt_i32_e32 vcc, 0, v2
	v_not_b32_e32 v2, v3
	s_nop 0
	v_cndmask_b32_e32 v192, v7, v6, vcc
	v_or_b32_e32 v6, 0x80000000, v3
	v_cmp_gt_i32_e32 vcc, 0, v3
	v_or_b32_e32 v3, 0x80000000, v4
	s_nop 0
	v_cndmask_b32_e32 v126, v6, v2, vcc
	v_not_b32_e32 v2, v4
	v_cmp_gt_i32_e32 vcc, 0, v4
	v_permlane32_swap_b32_e32 v192, v126
	s_nop 0
	v_cndmask_b32_e32 v155, v3, v2, vcc
	v_not_b32_e32 v2, v5
	v_or_b32_e32 v3, 0x80000000, v5
	v_cmp_gt_i32_e32 vcc, 0, v5
	s_nop 1
	v_cndmask_b32_e32 v102, v3, v2, vcc
	s_nop 1
	v_permlane32_swap_b32_e32 v155, v102

.LBB0_1160:
	s_barrier
	ds_read_b128 v[2:5], v1 offset:16384
	ds_read_b128 v[18:21], v1 offset:20480
	ds_read_b128 v[104:107], v67 offset:16384
	ds_read_b128 v[228:231], v67 offset:20480
	ds_read_b128 v[232:235], v69 offset:16384
	ds_read_b128 v[236:239], v69 offset:20480
	ds_read_b128 v[240:243], v92 offset:16384
	ds_read_b128 v[244:247], v92 offset:20480
	s_cmp_lt_u32 s2, 34
	s_cbranch_scc1 .LBB0_1162
	s_mov_b64 s[4:5], 0x22000
	v_lshl_add_u64 v[6:7], v[90:91], 0, s[4:5]
	s_add_i32 m0, s24, 0x2000
	s_nop 0
	global_load_lds_dwordx4 v[6:7], off
.LBB0_1162:
	s_waitcnt lgkmcnt(5)
	v_mfma_f32_32x32x16_bf16 v[2:17], v[62:65], v[2:5], 0
	v_mfma_f32_32x32x16_bf16 v[18:33], v[62:65], v[18:21], 0
	v_mfma_f32_32x32x16_bf16 v[2:17], v[58:61], v[104:107], v[2:17]
	s_waitcnt lgkmcnt(4)
	v_mfma_f32_32x32x16_bf16 v[18:33], v[58:61], v[228:231], v[18:33]
	s_waitcnt lgkmcnt(3)
	v_mfma_f32_32x32x16_bf16 v[2:17], v[54:57], v[232:235], v[2:17]
	s_waitcnt lgkmcnt(2)
	v_mfma_f32_32x32x16_bf16 v[18:33], v[54:57], v[236:239], v[18:33]
	s_waitcnt lgkmcnt(1)
	v_mfma_f32_32x32x16_bf16 v[2:17], v[50:53], v[240:243], v[2:17]
	s_waitcnt lgkmcnt(0)
	v_mfma_f32_32x32x16_bf16 v[18:33], v[50:53], v[244:247], v[18:33]
	s_nop 9
	v_max_i32_e32 v108, 0, v2
	v_max_i32_e32 v106, 0, v10
	v_max_i32_e32 v2, 0, v3
	v_max_i32_e32 v10, 0, v11
	v_max_i32_e32 v109, 0, v18
	v_pk_fma_f32 v[104:105], v[74:75], v[108:109], 0 op_sel_hi:[1,1,0]
	v_max_i32_e32 v107, 0, v26
	v_max_i32_e32 v3, 0, v19
	v_pk_fma_f32 v[106:107], v[76:77], v[106:107], 0 op_sel_hi:[1,1,0]
	v_pk_fma_f32 v[2:3], v[46:47], v[2:3], v[104:105]
	v_max_i32_e32 v11, 0, v27
	v_max_i32_e32 v18, 0, v4
	v_max_i32_e32 v19, 0, v20
	v_pk_fma_f32 v[10:11], v[42:43], v[10:11], v[106:107]
	v_pk_fma_f32 v[2:3], v[78:79], v[18:19], v[2:3]
	v_max_i32_e32 v18, 0, v12
	v_max_i32_e32 v19, 0, v28
	v_max_i32_e32 v4, 0, v5
	v_max_i32_e32 v5, 0, v21
	v_pk_fma_f32 v[10:11], v[80:81], v[18:19], v[10:11]
	v_pk_fma_f32 v[2:3], v[48:49], v[4:5], v[2:3]
	v_max_i32_e32 v4, 0, v13
	v_max_i32_e32 v5, 0, v29
	v_pk_fma_f32 v[4:5], v[44:45], v[4:5], v[10:11]
	v_max_i32_e32 v10, 0, v6
	v_max_i32_e32 v11, 0, v22
	v_pk_fma_f32 v[2:3], v[82:83], v[10:11], v[2:3]
	v_max_i32_e32 v10, 0, v14
	v_max_i32_e32 v11, 0, v30
	v_max_i32_e32 v6, 0, v7
	v_max_i32_e32 v7, 0, v23
	v_pk_fma_f32 v[4:5], v[84:85], v[10:11], v[4:5]
	v_pk_fma_f32 v[2:3], v[38:39], v[6:7], v[2:3]
	v_max_i32_e32 v6, 0, v15
	v_max_i32_e32 v7, 0, v31
	v_pk_fma_f32 v[4:5], v[34:35], v[6:7], v[4:5]
	v_max_i32_e32 v6, 0, v8
	v_max_i32_e32 v7, 0, v24
	v_pk_fma_f32 v[2:3], v[86:87], v[6:7], v[2:3]
	v_max_i32_e32 v6, 0, v16
	v_max_i32_e32 v7, 0, v32
	v_pk_fma_f32 v[4:5], v[88:89], v[6:7], v[4:5]
	v_max_i32_e32 v6, 0, v9
	v_max_i32_e32 v7, 0, v25
	v_pk_fma_f32 v[2:3], v[40:41], v[6:7], v[2:3]
	v_max_i32_e32 v6, 0, v17
	v_max_i32_e32 v7, 0, v33
	v_pk_fma_f32 v[4:5], v[36:37], v[6:7], v[4:5]
	v_not_b32_e32 v6, v2
	v_or_b32_e32 v7, 0x80000000, v2
	v_cmp_gt_i32_e32 vcc, 0, v2
	v_not_b32_e32 v2, v3
	s_nop 0
	v_cndmask_b32_e32 v193, v7, v6, vcc
	v_or_b32_e32 v6, 0x80000000, v3
	v_cmp_gt_i32_e32 vcc, 0, v3
	v_or_b32_e32 v3, 0x80000000, v4
	s_nop 0
	v_cndmask_b32_e32 v127, v6, v2, vcc
	v_not_b32_e32 v2, v4
	v_cmp_gt_i32_e32 vcc, 0, v4
	v_permlane32_swap_b32_e32 v193, v127
	s_nop 0
	v_cndmask_b32_e32 v156, v3, v2, vcc
	v_not_b32_e32 v2, v5
	v_or_b32_e32 v3, 0x80000000, v5
	v_cmp_gt_i32_e32 vcc, 0, v5
	s_nop 1
	v_cndmask_b32_e32 v103, v3, v2, vcc
	s_nop 1
	v_permlane32_swap_b32_e32 v156, v103

.LBB0_1186:
	s_barrier
	ds_read_b128 v[2:5], v1 offset:24576
	ds_read_b128 v[18:21], v1 offset:28672
	ds_read_b128 v[104:107], v67 offset:24576
	ds_read_b128 v[228:231], v67 offset:28672
	ds_read_b128 v[232:235], v69 offset:24576
	ds_read_b128 v[236:239], v69 offset:28672
	ds_read_b128 v[240:243], v92 offset:24576
	ds_read_b128 v[244:247], v92 offset:28672
	s_cmp_lt_u32 s2, 36
	s_cbranch_scc1 .LBB0_1188
	s_mov_b64 s[4:5], 0x24000
	v_lshl_add_u64 v[6:7], v[90:91], 0, s[4:5]
	s_add_i32 m0, s24, 0x4000
	s_nop 0
	global_load_lds_dwordx4 v[6:7], off
.LBB0_1188:
	s_waitcnt lgkmcnt(5)
	v_mfma_f32_32x32x16_bf16 v[2:17], v[62:65], v[2:5], 0
	v_mfma_f32_32x32x16_bf16 v[18:33], v[62:65], v[18:21], 0
	v_mfma_f32_32x32x16_bf16 v[2:17], v[58:61], v[104:107], v[2:17]
	s_waitcnt lgkmcnt(4)
	v_mfma_f32_32x32x16_bf16 v[18:33], v[58:61], v[228:231], v[18:33]
	s_waitcnt lgkmcnt(3)
	v_mfma_f32_32x32x16_bf16 v[2:17], v[54:57], v[232:235], v[2:17]
	s_waitcnt lgkmcnt(2)
	v_mfma_f32_32x32x16_bf16 v[18:33], v[54:57], v[236:239], v[18:33]
	s_waitcnt lgkmcnt(1)
	v_mfma_f32_32x32x16_bf16 v[2:17], v[50:53], v[240:243], v[2:17]
	s_waitcnt lgkmcnt(0)
	v_mfma_f32_32x32x16_bf16 v[18:33], v[50:53], v[244:247], v[18:33]
	s_nop 9
	v_max_i32_e32 v108, 0, v2
	v_max_i32_e32 v106, 0, v10
	v_max_i32_e32 v2, 0, v3
	v_max_i32_e32 v10, 0, v11
	v_max_i32_e32 v109, 0, v18
	v_pk_fma_f32 v[104:105], v[74:75], v[108:109], 0 op_sel_hi:[1,1,0]
	v_max_i32_e32 v107, 0, v26
	v_max_i32_e32 v3, 0, v19
	v_pk_fma_f32 v[106:107], v[76:77], v[106:107], 0 op_sel_hi:[1,1,0]
	v_pk_fma_f32 v[2:3], v[46:47], v[2:3], v[104:105]
	v_max_i32_e32 v11, 0, v27
	v_max_i32_e32 v18, 0, v4
	v_max_i32_e32 v19, 0, v20
	v_pk_fma_f32 v[10:11], v[42:43], v[10:11], v[106:107]
	v_pk_fma_f32 v[2:3], v[78:79], v[18:19], v[2:3]
	v_max_i32_e32 v18, 0, v12
	v_max_i32_e32 v19, 0, v28
	v_max_i32_e32 v4, 0, v5
	v_max_i32_e32 v5, 0, v21
	v_pk_fma_f32 v[10:11], v[80:81], v[18:19], v[10:11]
	v_pk_fma_f32 v[2:3], v[48:49], v[4:5], v[2:3]
	v_max_i32_e32 v4, 0, v13
	v_max_i32_e32 v5, 0, v29
	v_pk_fma_f32 v[4:5], v[44:45], v[4:5], v[10:11]
	v_max_i32_e32 v10, 0, v6
	v_max_i32_e32 v11, 0, v22
	v_pk_fma_f32 v[2:3], v[82:83], v[10:11], v[2:3]
	v_max_i32_e32 v10, 0, v14
	v_max_i32_e32 v11, 0, v30
	v_max_i32_e32 v6, 0, v7
	v_max_i32_e32 v7, 0, v23
	v_pk_fma_f32 v[4:5], v[84:85], v[10:11], v[4:5]
	v_pk_fma_f32 v[2:3], v[38:39], v[6:7], v[2:3]
	v_max_i32_e32 v6, 0, v15
	v_max_i32_e32 v7, 0, v31
	v_pk_fma_f32 v[4:5], v[34:35], v[6:7], v[4:5]
	v_max_i32_e32 v6, 0, v8
	v_max_i32_e32 v7, 0, v24
	v_pk_fma_f32 v[2:3], v[86:87], v[6:7], v[2:3]
	v_max_i32_e32 v6, 0, v16
	v_max_i32_e32 v7, 0, v32
	v_pk_fma_f32 v[4:5], v[88:89], v[6:7], v[4:5]
	v_max_i32_e32 v6, 0, v9
	v_max_i32_e32 v7, 0, v25
	v_pk_fma_f32 v[2:3], v[40:41], v[6:7], v[2:3]
	v_max_i32_e32 v6, 0, v17
	v_max_i32_e32 v7, 0, v33
	v_pk_fma_f32 v[4:5], v[36:37], v[6:7], v[4:5]
	v_not_b32_e32 v6, v2
	v_or_b32_e32 v7, 0x80000000, v2
	v_cmp_gt_i32_e32 vcc, 0, v2
	v_not_b32_e32 v2, v3
	s_nop 0
	v_cndmask_b32_e32 v194, v7, v6, vcc
	v_or_b32_e32 v6, 0x80000000, v3
	v_cmp_gt_i32_e32 vcc, 0, v3
	v_or_b32_e32 v3, 0x80000000, v4
	s_nop 0
	v_cndmask_b32_e32 v128, v6, v2, vcc
	v_not_b32_e32 v2, v4
	v_cmp_gt_i32_e32 vcc, 0, v4
	v_permlane32_swap_b32_e32 v194, v128
	s_nop 0
	v_cndmask_b32_e32 v157, v3, v2, vcc
	v_not_b32_e32 v2, v5
	v_or_b32_e32 v3, 0x80000000, v5
	v_cmp_gt_i32_e32 vcc, 0, v5
	s_nop 1
	v_cndmask_b32_e32 v104, v3, v2, vcc
	s_nop 1
	v_permlane32_swap_b32_e32 v157, v104

.LBB0_1212:
	s_barrier
	ds_read_b128 v[2:5], v1 offset:32768
	ds_read_b128 v[18:21], v1 offset:36864
	ds_read_b128 v[106:109], v67 offset:32768
	ds_read_b128 v[228:231], v67 offset:36864
	ds_read_b128 v[232:235], v69 offset:32768
	ds_read_b128 v[236:239], v69 offset:36864
	ds_read_b128 v[240:243], v92 offset:32768
	ds_read_b128 v[244:247], v92 offset:36864
	s_cmp_lt_u32 s2, 38
	s_cbranch_scc1 .LBB0_1214
	s_mov_b64 s[4:5], 0x26000
	v_lshl_add_u64 v[6:7], v[90:91], 0, s[4:5]
	s_add_i32 m0, s24, 0x6000
	s_nop 0
	global_load_lds_dwordx4 v[6:7], off
.LBB0_1214:
	s_waitcnt lgkmcnt(5)
	v_mfma_f32_32x32x16_bf16 v[2:17], v[62:65], v[2:5], 0
	v_mfma_f32_32x32x16_bf16 v[18:33], v[62:65], v[18:21], 0
	v_mfma_f32_32x32x16_bf16 v[2:17], v[58:61], v[106:109], v[2:17]
	s_waitcnt lgkmcnt(4)
	v_mfma_f32_32x32x16_bf16 v[18:33], v[58:61], v[228:231], v[18:33]
	s_waitcnt lgkmcnt(3)
	v_mfma_f32_32x32x16_bf16 v[2:17], v[54:57], v[232:235], v[2:17]
	s_waitcnt lgkmcnt(2)
	v_mfma_f32_32x32x16_bf16 v[18:33], v[54:57], v[236:239], v[18:33]
	s_waitcnt lgkmcnt(1)
	v_mfma_f32_32x32x16_bf16 v[2:17], v[50:53], v[240:243], v[2:17]
	s_waitcnt lgkmcnt(0)
	v_mfma_f32_32x32x16_bf16 v[18:33], v[50:53], v[244:247], v[18:33]
	s_nop 9
	v_max_i32_e32 v130, 0, v2
	v_max_i32_e32 v108, 0, v10
	v_max_i32_e32 v2, 0, v3
	v_max_i32_e32 v10, 0, v11
	v_max_i32_e32 v131, 0, v18
	v_pk_fma_f32 v[106:107], v[74:75], v[130:131], 0 op_sel_hi:[1,1,0]
	v_max_i32_e32 v109, 0, v26
	v_max_i32_e32 v3, 0, v19
	v_pk_fma_f32 v[108:109], v[76:77], v[108:109], 0 op_sel_hi:[1,1,0]
	v_pk_fma_f32 v[2:3], v[46:47], v[2:3], v[106:107]
	v_max_i32_e32 v11, 0, v27
	v_max_i32_e32 v18, 0, v4
	v_max_i32_e32 v19, 0, v20
	v_pk_fma_f32 v[10:11], v[42:43], v[10:11], v[108:109]
	v_pk_fma_f32 v[2:3], v[78:79], v[18:19], v[2:3]
	v_max_i32_e32 v18, 0, v12
	v_max_i32_e32 v19, 0, v28
	v_max_i32_e32 v4, 0, v5
	v_max_i32_e32 v5, 0, v21
	v_pk_fma_f32 v[10:11], v[80:81], v[18:19], v[10:11]
	v_pk_fma_f32 v[2:3], v[48:49], v[4:5], v[2:3]
	v_max_i32_e32 v4, 0, v13
	v_max_i32_e32 v5, 0, v29
	v_pk_fma_f32 v[4:5], v[44:45], v[4:5], v[10:11]
	v_max_i32_e32 v10, 0, v6
	v_max_i32_e32 v11, 0, v22
	v_pk_fma_f32 v[2:3], v[82:83], v[10:11], v[2:3]
	v_max_i32_e32 v10, 0, v14
	v_max_i32_e32 v11, 0, v30
	v_max_i32_e32 v6, 0, v7
	v_max_i32_e32 v7, 0, v23
	v_pk_fma_f32 v[4:5], v[84:85], v[10:11], v[4:5]
	v_pk_fma_f32 v[2:3], v[38:39], v[6:7], v[2:3]
	v_max_i32_e32 v6, 0, v15
	v_max_i32_e32 v7, 0, v31
	v_pk_fma_f32 v[4:5], v[34:35], v[6:7], v[4:5]
	v_max_i32_e32 v6, 0, v8
	v_max_i32_e32 v7, 0, v24
	v_pk_fma_f32 v[2:3], v[86:87], v[6:7], v[2:3]
	v_max_i32_e32 v6, 0, v16
	v_max_i32_e32 v7, 0, v32
	v_pk_fma_f32 v[4:5], v[88:89], v[6:7], v[4:5]
	v_max_i32_e32 v6, 0, v9
	v_max_i32_e32 v7, 0, v25
	v_pk_fma_f32 v[2:3], v[40:41], v[6:7], v[2:3]
	v_max_i32_e32 v6, 0, v17
	v_max_i32_e32 v7, 0, v33
	v_pk_fma_f32 v[4:5], v[36:37], v[6:7], v[4:5]
	v_not_b32_e32 v6, v2
	v_or_b32_e32 v7, 0x80000000, v2
	v_cmp_gt_i32_e32 vcc, 0, v2
	v_not_b32_e32 v2, v3
	s_nop 0
	v_cndmask_b32_e32 v195, v7, v6, vcc
	v_or_b32_e32 v6, 0x80000000, v3
	v_cmp_gt_i32_e32 vcc, 0, v3
	v_or_b32_e32 v3, 0x80000000, v4
	s_nop 0
	v_cndmask_b32_e32 v129, v6, v2, vcc
	v_not_b32_e32 v2, v4
	v_cmp_gt_i32_e32 vcc, 0, v4
	v_permlane32_swap_b32_e32 v195, v129
	s_nop 0
	v_cndmask_b32_e32 v158, v3, v2, vcc
	v_not_b32_e32 v2, v5
	v_or_b32_e32 v3, 0x80000000, v5
	v_cmp_gt_i32_e32 vcc, 0, v5
	s_nop 1
	v_cndmask_b32_e32 v105, v3, v2, vcc
	s_nop 1
	v_permlane32_swap_b32_e32 v158, v105

.LBB0_1238:
	s_barrier
	ds_read_b128 v[2:5], v1 offset:40960
	ds_read_b128 v[18:21], v1 offset:45056
	ds_read_b128 v[106:109], v67 offset:40960
	ds_read_b128 v[228:231], v67 offset:45056
	ds_read_b128 v[232:235], v69 offset:40960
	ds_read_b128 v[236:239], v69 offset:45056
	ds_read_b128 v[240:243], v92 offset:40960
	ds_read_b128 v[244:247], v92 offset:45056
	s_cmp_lt_u32 s2, 40
	s_cbranch_scc1 .LBB0_1240
	s_mov_b64 s[4:5], 0x28000
	v_lshl_add_u64 v[6:7], v[90:91], 0, s[4:5]
	s_add_i32 m0, s24, 0x8000
	s_nop 0
	global_load_lds_dwordx4 v[6:7], off
.LBB0_1240:
	s_waitcnt lgkmcnt(5)
	v_mfma_f32_32x32x16_bf16 v[2:17], v[62:65], v[2:5], 0
	v_mfma_f32_32x32x16_bf16 v[18:33], v[62:65], v[18:21], 0
	v_mfma_f32_32x32x16_bf16 v[2:17], v[58:61], v[106:109], v[2:17]
	s_waitcnt lgkmcnt(4)
	v_mfma_f32_32x32x16_bf16 v[18:33], v[58:61], v[228:231], v[18:33]
	s_waitcnt lgkmcnt(3)
	v_mfma_f32_32x32x16_bf16 v[2:17], v[54:57], v[232:235], v[2:17]
	s_waitcnt lgkmcnt(2)
	v_mfma_f32_32x32x16_bf16 v[18:33], v[54:57], v[236:239], v[18:33]
	s_waitcnt lgkmcnt(1)
	v_mfma_f32_32x32x16_bf16 v[2:17], v[50:53], v[240:243], v[2:17]
	s_waitcnt lgkmcnt(0)
	v_mfma_f32_32x32x16_bf16 v[18:33], v[50:53], v[244:247], v[18:33]
	s_nop 9
	v_max_i32_e32 v130, 0, v2
	v_max_i32_e32 v108, 0, v10
	v_max_i32_e32 v2, 0, v3
	v_max_i32_e32 v10, 0, v11
	v_max_i32_e32 v131, 0, v18
	v_pk_fma_f32 v[106:107], v[74:75], v[130:131], 0 op_sel_hi:[1,1,0]
	v_max_i32_e32 v109, 0, v26
	v_max_i32_e32 v3, 0, v19
	v_pk_fma_f32 v[108:109], v[76:77], v[108:109], 0 op_sel_hi:[1,1,0]
	v_pk_fma_f32 v[2:3], v[46:47], v[2:3], v[106:107]
	v_max_i32_e32 v11, 0, v27
	v_max_i32_e32 v18, 0, v4
	v_max_i32_e32 v19, 0, v20
	v_pk_fma_f32 v[10:11], v[42:43], v[10:11], v[108:109]
	v_pk_fma_f32 v[2:3], v[78:79], v[18:19], v[2:3]
	v_max_i32_e32 v18, 0, v12
	v_max_i32_e32 v19, 0, v28
	v_max_i32_e32 v4, 0, v5
	v_max_i32_e32 v5, 0, v21
	v_pk_fma_f32 v[10:11], v[80:81], v[18:19], v[10:11]
	v_pk_fma_f32 v[2:3], v[48:49], v[4:5], v[2:3]
	v_max_i32_e32 v4, 0, v13
	v_max_i32_e32 v5, 0, v29
	v_pk_fma_f32 v[4:5], v[44:45], v[4:5], v[10:11]
	v_max_i32_e32 v10, 0, v6
	v_max_i32_e32 v11, 0, v22
	v_pk_fma_f32 v[2:3], v[82:83], v[10:11], v[2:3]
	v_max_i32_e32 v10, 0, v14
	v_max_i32_e32 v11, 0, v30
	v_max_i32_e32 v6, 0, v7
	v_max_i32_e32 v7, 0, v23
	v_pk_fma_f32 v[4:5], v[84:85], v[10:11], v[4:5]
	v_pk_fma_f32 v[2:3], v[38:39], v[6:7], v[2:3]
	v_max_i32_e32 v6, 0, v15
	v_max_i32_e32 v7, 0, v31
	v_pk_fma_f32 v[4:5], v[34:35], v[6:7], v[4:5]
	v_max_i32_e32 v6, 0, v8
	v_max_i32_e32 v7, 0, v24
	v_pk_fma_f32 v[2:3], v[86:87], v[6:7], v[2:3]
	v_max_i32_e32 v6, 0, v16
	v_max_i32_e32 v7, 0, v32
	v_pk_fma_f32 v[4:5], v[88:89], v[6:7], v[4:5]
	v_max_i32_e32 v6, 0, v9
	v_max_i32_e32 v7, 0, v25
	v_pk_fma_f32 v[2:3], v[40:41], v[6:7], v[2:3]
	v_max_i32_e32 v6, 0, v17
	v_max_i32_e32 v7, 0, v33
	v_pk_fma_f32 v[4:5], v[36:37], v[6:7], v[4:5]
	v_not_b32_e32 v6, v2
	v_or_b32_e32 v7, 0x80000000, v2
	v_cmp_gt_i32_e32 vcc, 0, v2
	v_not_b32_e32 v2, v3
	s_nop 0
	v_cndmask_b32_e32 v196, v7, v6, vcc
	v_or_b32_e32 v6, 0x80000000, v3
	v_cmp_gt_i32_e32 vcc, 0, v3
	v_or_b32_e32 v3, 0x80000000, v4
	s_nop 0
	v_cndmask_b32_e32 v130, v6, v2, vcc
	v_not_b32_e32 v2, v4
	v_cmp_gt_i32_e32 vcc, 0, v4
	v_permlane32_swap_b32_e32 v196, v130
	s_nop 0
	v_cndmask_b32_e32 v159, v3, v2, vcc
	v_not_b32_e32 v2, v5
	v_or_b32_e32 v3, 0x80000000, v5
	v_cmp_gt_i32_e32 vcc, 0, v5
	s_nop 1
	v_cndmask_b32_e32 v106, v3, v2, vcc
	s_nop 1
	v_permlane32_swap_b32_e32 v159, v106

.LBB0_1264:
	s_barrier
	ds_read_b128 v[2:5], v1 offset:49152
	ds_read_b128 v[18:21], v1 offset:53248
	ds_read_b128 v[132:135], v67 offset:49152
	ds_read_b128 v[228:231], v67 offset:53248
	ds_read_b128 v[232:235], v69 offset:49152
	ds_read_b128 v[236:239], v69 offset:53248
	ds_read_b128 v[240:243], v92 offset:49152
	ds_read_b128 v[244:247], v92 offset:53248
	s_cmp_lt_u32 s2, 42
	s_cbranch_scc1 .LBB0_1266
	s_mov_b64 s[4:5], 0x2a000
	v_lshl_add_u64 v[6:7], v[90:91], 0, s[4:5]
	s_add_i32 m0, s24, 0xa000
	s_nop 0
	global_load_lds_dwordx4 v[6:7], off
.LBB0_1266:
	s_waitcnt lgkmcnt(5)
	v_mfma_f32_32x32x16_bf16 v[2:17], v[62:65], v[2:5], 0
	v_mfma_f32_32x32x16_bf16 v[18:33], v[62:65], v[18:21], 0
	v_mfma_f32_32x32x16_bf16 v[2:17], v[58:61], v[132:135], v[2:17]
	s_waitcnt lgkmcnt(4)
	v_mfma_f32_32x32x16_bf16 v[18:33], v[58:61], v[228:231], v[18:33]
	s_waitcnt lgkmcnt(3)
	v_mfma_f32_32x32x16_bf16 v[2:17], v[54:57], v[232:235], v[2:17]
	s_waitcnt lgkmcnt(2)
	v_mfma_f32_32x32x16_bf16 v[18:33], v[54:57], v[236:239], v[18:33]
	s_waitcnt lgkmcnt(1)
	v_mfma_f32_32x32x16_bf16 v[2:17], v[50:53], v[240:243], v[2:17]
	s_waitcnt lgkmcnt(0)
	v_mfma_f32_32x32x16_bf16 v[18:33], v[50:53], v[244:247], v[18:33]
	s_nop 9
	v_max_i32_e32 v108, 0, v2
	v_max_i32_e32 v132, 0, v10
	v_max_i32_e32 v2, 0, v3
	v_max_i32_e32 v10, 0, v11
	v_max_i32_e32 v109, 0, v18
	v_pk_fma_f32 v[108:109], v[74:75], v[108:109], 0 op_sel_hi:[1,1,0]
	v_max_i32_e32 v133, 0, v26
	v_max_i32_e32 v3, 0, v19
	v_pk_fma_f32 v[132:133], v[76:77], v[132:133], 0 op_sel_hi:[1,1,0]
	v_pk_fma_f32 v[2:3], v[46:47], v[2:3], v[108:109]
	v_max_i32_e32 v11, 0, v27
	v_max_i32_e32 v18, 0, v4
	v_max_i32_e32 v19, 0, v20
	v_pk_fma_f32 v[10:11], v[42:43], v[10:11], v[132:133]
	v_pk_fma_f32 v[2:3], v[78:79], v[18:19], v[2:3]
	v_max_i32_e32 v18, 0, v12
	v_max_i32_e32 v19, 0, v28
	v_max_i32_e32 v4, 0, v5
	v_max_i32_e32 v5, 0, v21
	v_pk_fma_f32 v[10:11], v[80:81], v[18:19], v[10:11]
	v_pk_fma_f32 v[2:3], v[48:49], v[4:5], v[2:3]
	v_max_i32_e32 v4, 0, v13
	v_max_i32_e32 v5, 0, v29
	v_pk_fma_f32 v[4:5], v[44:45], v[4:5], v[10:11]
	v_max_i32_e32 v10, 0, v6
	v_max_i32_e32 v11, 0, v22
	v_pk_fma_f32 v[2:3], v[82:83], v[10:11], v[2:3]
	v_max_i32_e32 v10, 0, v14
	v_max_i32_e32 v11, 0, v30
	v_max_i32_e32 v6, 0, v7
	v_max_i32_e32 v7, 0, v23
	v_pk_fma_f32 v[4:5], v[84:85], v[10:11], v[4:5]
	v_pk_fma_f32 v[2:3], v[38:39], v[6:7], v[2:3]
	v_max_i32_e32 v6, 0, v15
	v_max_i32_e32 v7, 0, v31
	v_pk_fma_f32 v[4:5], v[34:35], v[6:7], v[4:5]
	v_max_i32_e32 v6, 0, v8
	v_max_i32_e32 v7, 0, v24
	v_pk_fma_f32 v[2:3], v[86:87], v[6:7], v[2:3]
	v_max_i32_e32 v6, 0, v16
	v_max_i32_e32 v7, 0, v32
	v_pk_fma_f32 v[4:5], v[88:89], v[6:7], v[4:5]
	v_max_i32_e32 v6, 0, v9
	v_max_i32_e32 v7, 0, v25
	v_pk_fma_f32 v[2:3], v[40:41], v[6:7], v[2:3]
	v_max_i32_e32 v6, 0, v17
	v_max_i32_e32 v7, 0, v33
	v_pk_fma_f32 v[4:5], v[36:37], v[6:7], v[4:5]
	v_not_b32_e32 v6, v2
	v_or_b32_e32 v7, 0x80000000, v2
	v_cmp_gt_i32_e32 vcc, 0, v2
	v_not_b32_e32 v2, v3
	s_nop 0
	v_cndmask_b32_e32 v198, v7, v6, vcc
	v_or_b32_e32 v6, 0x80000000, v3
	v_cmp_gt_i32_e32 vcc, 0, v3
	v_or_b32_e32 v3, 0x80000000, v4
	s_nop 0
	v_cndmask_b32_e32 v132, v6, v2, vcc
	v_not_b32_e32 v2, v4
	v_cmp_gt_i32_e32 vcc, 0, v4
	v_permlane32_swap_b32_e32 v198, v132
	s_nop 0
	v_cndmask_b32_e32 v161, v3, v2, vcc
	v_not_b32_e32 v2, v5
	v_or_b32_e32 v3, 0x80000000, v5
	v_cmp_gt_i32_e32 vcc, 0, v5
	s_nop 1
	v_cndmask_b32_e32 v107, v3, v2, vcc
	s_nop 1
	v_permlane32_swap_b32_e32 v161, v107

.LBB0_1290:
	s_barrier
	ds_read_b128 v[2:5], v1 offset:57344
	ds_read_b128 v[18:21], v1 offset:61440
	ds_read_b128 v[134:137], v67 offset:57344
	ds_read_b128 v[228:231], v67 offset:61440
	ds_read_b128 v[232:235], v69 offset:57344
	ds_read_b128 v[236:239], v69 offset:61440
	ds_read_b128 v[240:243], v92 offset:57344
	ds_read_b128 v[244:247], v92 offset:61440
	s_cmp_lt_u32 s2, 44
	s_cbranch_scc1 .LBB0_1292
	s_mov_b64 s[4:5], 0x2c000
	v_lshl_add_u64 v[6:7], v[90:91], 0, s[4:5]
	s_add_i32 m0, s24, 0xc000
	s_nop 0
	global_load_lds_dwordx4 v[6:7], off
.LBB0_1292:
	s_waitcnt lgkmcnt(5)
	v_mfma_f32_32x32x16_bf16 v[2:17], v[62:65], v[2:5], 0
	v_mfma_f32_32x32x16_bf16 v[18:33], v[62:65], v[18:21], 0
	v_mfma_f32_32x32x16_bf16 v[2:17], v[58:61], v[134:137], v[2:17]
	s_waitcnt lgkmcnt(4)
	v_mfma_f32_32x32x16_bf16 v[18:33], v[58:61], v[228:231], v[18:33]
	s_waitcnt lgkmcnt(3)
	v_mfma_f32_32x32x16_bf16 v[2:17], v[54:57], v[232:235], v[2:17]
	s_waitcnt lgkmcnt(2)
	v_mfma_f32_32x32x16_bf16 v[18:33], v[54:57], v[236:239], v[18:33]
	s_waitcnt lgkmcnt(1)
	v_mfma_f32_32x32x16_bf16 v[2:17], v[50:53], v[240:243], v[2:17]
	s_waitcnt lgkmcnt(0)
	v_mfma_f32_32x32x16_bf16 v[18:33], v[50:53], v[244:247], v[18:33]
	s_nop 9
	v_max_i32_e32 v108, 0, v2
	v_max_i32_e32 v134, 0, v10
	v_max_i32_e32 v2, 0, v3
	v_max_i32_e32 v10, 0, v11
	v_max_i32_e32 v109, 0, v18
	v_pk_fma_f32 v[108:109], v[74:75], v[108:109], 0 op_sel_hi:[1,1,0]
	v_max_i32_e32 v135, 0, v26
	v_max_i32_e32 v3, 0, v19
	v_pk_fma_f32 v[134:135], v[76:77], v[134:135], 0 op_sel_hi:[1,1,0]
	v_pk_fma_f32 v[2:3], v[46:47], v[2:3], v[108:109]
	v_max_i32_e32 v11, 0, v27
	v_max_i32_e32 v18, 0, v4
	v_max_i32_e32 v19, 0, v20
	v_pk_fma_f32 v[10:11], v[42:43], v[10:11], v[134:135]
	v_pk_fma_f32 v[2:3], v[78:79], v[18:19], v[2:3]
	v_max_i32_e32 v18, 0, v12
	v_max_i32_e32 v19, 0, v28
	v_max_i32_e32 v4, 0, v5
	v_max_i32_e32 v5, 0, v21
	v_pk_fma_f32 v[10:11], v[80:81], v[18:19], v[10:11]
	v_pk_fma_f32 v[2:3], v[48:49], v[4:5], v[2:3]
	v_max_i32_e32 v4, 0, v13
	v_max_i32_e32 v5, 0, v29
	v_pk_fma_f32 v[4:5], v[44:45], v[4:5], v[10:11]
	v_max_i32_e32 v10, 0, v6
	v_max_i32_e32 v11, 0, v22
	v_pk_fma_f32 v[2:3], v[82:83], v[10:11], v[2:3]
	v_max_i32_e32 v10, 0, v14
	v_max_i32_e32 v11, 0, v30
	v_max_i32_e32 v6, 0, v7
	v_max_i32_e32 v7, 0, v23
	v_pk_fma_f32 v[4:5], v[84:85], v[10:11], v[4:5]
	v_pk_fma_f32 v[2:3], v[38:39], v[6:7], v[2:3]
	v_max_i32_e32 v6, 0, v15
	v_max_i32_e32 v7, 0, v31
	v_pk_fma_f32 v[4:5], v[34:35], v[6:7], v[4:5]
	v_max_i32_e32 v6, 0, v8
	v_max_i32_e32 v7, 0, v24
	v_pk_fma_f32 v[2:3], v[86:87], v[6:7], v[2:3]
	v_max_i32_e32 v6, 0, v16
	v_max_i32_e32 v7, 0, v32
	v_pk_fma_f32 v[4:5], v[88:89], v[6:7], v[4:5]
	v_max_i32_e32 v6, 0, v9
	v_max_i32_e32 v7, 0, v25
	v_pk_fma_f32 v[2:3], v[40:41], v[6:7], v[2:3]
	v_max_i32_e32 v6, 0, v17
	v_max_i32_e32 v7, 0, v33
	v_pk_fma_f32 v[4:5], v[36:37], v[6:7], v[4:5]
	v_not_b32_e32 v6, v2
	v_or_b32_e32 v7, 0x80000000, v2
	v_cmp_gt_i32_e32 vcc, 0, v2
	v_not_b32_e32 v2, v3
	s_nop 0
	v_cndmask_b32_e32 v200, v7, v6, vcc
	v_or_b32_e32 v6, 0x80000000, v3
	v_cmp_gt_i32_e32 vcc, 0, v3
	v_or_b32_e32 v3, 0x80000000, v4
	s_nop 0
	v_cndmask_b32_e32 v133, v6, v2, vcc
	v_not_b32_e32 v2, v4
	v_cmp_gt_i32_e32 vcc, 0, v4
	v_permlane32_swap_b32_e32 v200, v133
	s_nop 0
	v_cndmask_b32_e32 v164, v3, v2, vcc
	v_not_b32_e32 v2, v5
	v_or_b32_e32 v3, 0x80000000, v5
	v_cmp_gt_i32_e32 vcc, 0, v5
	s_nop 1
	v_cndmask_b32_e32 v108, v3, v2, vcc
	s_nop 1
	v_permlane32_swap_b32_e32 v164, v108

.LBB0_1316:
	s_barrier
	ds_read_b128 v[2:5], v1
	ds_read_b128 v[18:21], v1 offset:4096
	ds_read_b128 v[134:137], v67
	ds_read_b128 v[228:231], v67 offset:4096
	ds_read_b128 v[232:235], v69
	ds_read_b128 v[236:239], v69 offset:4096
	ds_read_b128 v[240:243], v92
	ds_read_b128 v[244:247], v92 offset:4096
	s_cmp_lt_u32 s2, 46
	s_cbranch_scc1 .LBB0_1318
	s_mov_b64 s[4:5], 0x2e000
	v_lshl_add_u64 v[6:7], v[90:91], 0, s[4:5]
	s_add_i32 m0, s24, 0xe000
	s_nop 0
	global_load_lds_dwordx4 v[6:7], off
.LBB0_1318:
	s_waitcnt lgkmcnt(5)
	v_mfma_f32_32x32x16_bf16 v[2:17], v[62:65], v[2:5], 0
	v_mfma_f32_32x32x16_bf16 v[18:33], v[62:65], v[18:21], 0
	v_mfma_f32_32x32x16_bf16 v[2:17], v[58:61], v[134:137], v[2:17]
	s_waitcnt lgkmcnt(4)
	v_mfma_f32_32x32x16_bf16 v[18:33], v[58:61], v[228:231], v[18:33]
	s_waitcnt lgkmcnt(3)
	v_mfma_f32_32x32x16_bf16 v[2:17], v[54:57], v[232:235], v[2:17]
	s_waitcnt lgkmcnt(2)
	v_mfma_f32_32x32x16_bf16 v[18:33], v[54:57], v[236:239], v[18:33]
	s_waitcnt lgkmcnt(1)
	v_mfma_f32_32x32x16_bf16 v[2:17], v[50:53], v[240:243], v[2:17]
	s_waitcnt lgkmcnt(0)
	v_mfma_f32_32x32x16_bf16 v[18:33], v[50:53], v[244:247], v[18:33]
	s_nop 9
	v_max_i32_e32 v138, 0, v2
	v_max_i32_e32 v136, 0, v10
	v_max_i32_e32 v2, 0, v3
	v_max_i32_e32 v10, 0, v11
	v_max_i32_e32 v139, 0, v18
	v_pk_fma_f32 v[134:135], v[74:75], v[138:139], 0 op_sel_hi:[1,1,0]
	v_max_i32_e32 v137, 0, v26
	v_max_i32_e32 v3, 0, v19
	v_pk_fma_f32 v[136:137], v[76:77], v[136:137], 0 op_sel_hi:[1,1,0]
	v_pk_fma_f32 v[2:3], v[46:47], v[2:3], v[134:135]
	v_max_i32_e32 v11, 0, v27
	v_max_i32_e32 v18, 0, v4
	v_max_i32_e32 v19, 0, v20
	v_pk_fma_f32 v[10:11], v[42:43], v[10:11], v[136:137]
	v_pk_fma_f32 v[2:3], v[78:79], v[18:19], v[2:3]
	v_max_i32_e32 v18, 0, v12
	v_max_i32_e32 v19, 0, v28
	v_max_i32_e32 v4, 0, v5
	v_max_i32_e32 v5, 0, v21
	v_pk_fma_f32 v[10:11], v[80:81], v[18:19], v[10:11]
	v_pk_fma_f32 v[2:3], v[48:49], v[4:5], v[2:3]
	v_max_i32_e32 v4, 0, v13
	v_max_i32_e32 v5, 0, v29
	v_pk_fma_f32 v[4:5], v[44:45], v[4:5], v[10:11]
	v_max_i32_e32 v10, 0, v6
	v_max_i32_e32 v11, 0, v22
	v_pk_fma_f32 v[2:3], v[82:83], v[10:11], v[2:3]
	v_max_i32_e32 v10, 0, v14
	v_max_i32_e32 v11, 0, v30
	v_max_i32_e32 v6, 0, v7
	v_max_i32_e32 v7, 0, v23
	v_pk_fma_f32 v[4:5], v[84:85], v[10:11], v[4:5]
	v_pk_fma_f32 v[2:3], v[38:39], v[6:7], v[2:3]
	v_max_i32_e32 v6, 0, v15
	v_max_i32_e32 v7, 0, v31
	v_pk_fma_f32 v[4:5], v[34:35], v[6:7], v[4:5]
	v_max_i32_e32 v6, 0, v8
	v_max_i32_e32 v7, 0, v24
	v_pk_fma_f32 v[2:3], v[86:87], v[6:7], v[2:3]
	v_max_i32_e32 v6, 0, v16
	v_max_i32_e32 v7, 0, v32
	v_pk_fma_f32 v[4:5], v[88:89], v[6:7], v[4:5]
	v_max_i32_e32 v6, 0, v9
	v_max_i32_e32 v7, 0, v25
	v_pk_fma_f32 v[2:3], v[40:41], v[6:7], v[2:3]
	v_max_i32_e32 v6, 0, v17
	v_max_i32_e32 v7, 0, v33
	v_pk_fma_f32 v[4:5], v[36:37], v[6:7], v[4:5]
	v_not_b32_e32 v6, v2
	v_or_b32_e32 v7, 0x80000000, v2
	v_cmp_gt_i32_e32 vcc, 0, v2
	v_not_b32_e32 v2, v3
	s_nop 0
	v_cndmask_b32_e32 v206, v7, v6, vcc
	v_or_b32_e32 v6, 0x80000000, v3
	v_cmp_gt_i32_e32 vcc, 0, v3
	v_or_b32_e32 v3, 0x80000000, v4
	s_nop 0
	v_cndmask_b32_e32 v138, v6, v2, vcc
	v_not_b32_e32 v2, v4
	v_cmp_gt_i32_e32 vcc, 0, v4
	v_permlane32_swap_b32_e32 v206, v138
	s_nop 0
	v_cndmask_b32_e32 v170, v3, v2, vcc
	v_not_b32_e32 v2, v5
	v_or_b32_e32 v3, 0x80000000, v5
	v_cmp_gt_i32_e32 vcc, 0, v5
	s_nop 1
	v_cndmask_b32_e32 v109, v3, v2, vcc
	s_nop 1
	v_permlane32_swap_b32_e32 v170, v109

.LBB0_1342:
	s_barrier
	ds_read_b128 v[2:5], v1 offset:8192
	ds_read_b128 v[18:21], v1 offset:12288
	ds_read_b128 v[134:137], v67 offset:8192
	ds_read_b128 v[228:231], v67 offset:12288
	ds_read_b128 v[232:235], v69 offset:8192
	ds_read_b128 v[236:239], v69 offset:12288
	ds_read_b128 v[240:243], v92 offset:8192
	ds_read_b128 v[244:247], v92 offset:12288
	s_cmp_lt_u32 s2, 48
	s_cbranch_scc1 .LBB0_1344
	s_mov_b64 s[4:5], 0x30000
	v_lshl_add_u64 v[6:7], v[90:91], 0, s[4:5]
	s_mov_b32 m0, s24
	s_nop 0
	global_load_lds_dwordx4 v[6:7], off
.LBB0_1344:
	s_waitcnt lgkmcnt(5)
	v_mfma_f32_32x32x16_bf16 v[2:17], v[62:65], v[2:5], 0
	v_mfma_f32_32x32x16_bf16 v[18:33], v[62:65], v[18:21], 0
	v_mfma_f32_32x32x16_bf16 v[2:17], v[58:61], v[134:137], v[2:17]
	s_waitcnt lgkmcnt(4)
	v_mfma_f32_32x32x16_bf16 v[18:33], v[58:61], v[228:231], v[18:33]
	s_waitcnt lgkmcnt(3)
	v_mfma_f32_32x32x16_bf16 v[2:17], v[54:57], v[232:235], v[2:17]
	s_waitcnt lgkmcnt(2)
	v_mfma_f32_32x32x16_bf16 v[18:33], v[54:57], v[236:239], v[18:33]
	s_waitcnt lgkmcnt(1)
	v_mfma_f32_32x32x16_bf16 v[2:17], v[50:53], v[240:243], v[2:17]
	s_waitcnt lgkmcnt(0)
	v_mfma_f32_32x32x16_bf16 v[18:33], v[50:53], v[244:247], v[18:33]
	s_nop 9
	v_max_i32_e32 v166, 0, v2
	v_max_i32_e32 v136, 0, v10
	v_max_i32_e32 v2, 0, v3
	v_max_i32_e32 v10, 0, v11
	v_max_i32_e32 v167, 0, v18
	v_pk_fma_f32 v[134:135], v[74:75], v[166:167], 0 op_sel_hi:[1,1,0]
	v_max_i32_e32 v137, 0, v26
	v_max_i32_e32 v3, 0, v19
	v_pk_fma_f32 v[136:137], v[76:77], v[136:137], 0 op_sel_hi:[1,1,0]
	v_pk_fma_f32 v[2:3], v[46:47], v[2:3], v[134:135]
	v_max_i32_e32 v11, 0, v27
	v_max_i32_e32 v18, 0, v4
	v_max_i32_e32 v19, 0, v20
	v_pk_fma_f32 v[10:11], v[42:43], v[10:11], v[136:137]
	v_pk_fma_f32 v[2:3], v[78:79], v[18:19], v[2:3]
	v_max_i32_e32 v18, 0, v12
	v_max_i32_e32 v19, 0, v28
	v_max_i32_e32 v4, 0, v5
	v_max_i32_e32 v5, 0, v21
	v_pk_fma_f32 v[10:11], v[80:81], v[18:19], v[10:11]
	v_pk_fma_f32 v[2:3], v[48:49], v[4:5], v[2:3]
	v_max_i32_e32 v4, 0, v13
	v_max_i32_e32 v5, 0, v29
	v_pk_fma_f32 v[4:5], v[44:45], v[4:5], v[10:11]
	v_max_i32_e32 v10, 0, v6
	v_max_i32_e32 v11, 0, v22
	v_pk_fma_f32 v[2:3], v[82:83], v[10:11], v[2:3]
	v_max_i32_e32 v10, 0, v14
	v_max_i32_e32 v11, 0, v30
	v_max_i32_e32 v6, 0, v7
	v_max_i32_e32 v7, 0, v23
	v_pk_fma_f32 v[4:5], v[84:85], v[10:11], v[4:5]
	v_pk_fma_f32 v[2:3], v[38:39], v[6:7], v[2:3]
	v_max_i32_e32 v6, 0, v15
	v_max_i32_e32 v7, 0, v31
	v_pk_fma_f32 v[4:5], v[34:35], v[6:7], v[4:5]
	v_max_i32_e32 v6, 0, v8
	v_max_i32_e32 v7, 0, v24
	v_pk_fma_f32 v[2:3], v[86:87], v[6:7], v[2:3]
	v_max_i32_e32 v6, 0, v16
	v_max_i32_e32 v7, 0, v32
	v_pk_fma_f32 v[4:5], v[88:89], v[6:7], v[4:5]
	v_max_i32_e32 v6, 0, v9
	v_max_i32_e32 v7, 0, v25
	v_pk_fma_f32 v[2:3], v[40:41], v[6:7], v[2:3]
	v_max_i32_e32 v6, 0, v17
	v_max_i32_e32 v7, 0, v33
	v_pk_fma_f32 v[4:5], v[36:37], v[6:7], v[4:5]
	v_not_b32_e32 v6, v2
	v_or_b32_e32 v7, 0x80000000, v2
	v_cmp_gt_i32_e32 vcc, 0, v2
	v_not_b32_e32 v2, v3
	s_nop 0
	v_cndmask_b32_e32 v207, v7, v6, vcc
	v_or_b32_e32 v6, 0x80000000, v3
	v_cmp_gt_i32_e32 vcc, 0, v3
	v_or_b32_e32 v3, 0x80000000, v4
	s_nop 0
	v_cndmask_b32_e32 v139, v6, v2, vcc
	v_not_b32_e32 v2, v4
	v_cmp_gt_i32_e32 vcc, 0, v4
	v_permlane32_swap_b32_e32 v207, v139
	s_nop 0
	v_cndmask_b32_e32 v171, v3, v2, vcc
	v_not_b32_e32 v2, v5
	v_or_b32_e32 v3, 0x80000000, v5
	v_cmp_gt_i32_e32 vcc, 0, v5
	s_nop 1
	v_cndmask_b32_e32 v110, v3, v2, vcc
	s_nop 1
	v_permlane32_swap_b32_e32 v171, v110

.LBB0_1368:
	s_barrier
	ds_read_b128 v[2:5], v1 offset:16384
	ds_read_b128 v[18:21], v1 offset:20480
	ds_read_b128 v[134:137], v67 offset:16384
	ds_read_b128 v[228:231], v67 offset:20480
	ds_read_b128 v[232:235], v69 offset:16384
	ds_read_b128 v[236:239], v69 offset:20480
	ds_read_b128 v[240:243], v92 offset:16384
	ds_read_b128 v[244:247], v92 offset:20480
	s_cmp_lt_u32 s2, 50
	s_cbranch_scc1 .LBB0_1370
	s_mov_b64 s[4:5], 0x32000
	v_lshl_add_u64 v[6:7], v[90:91], 0, s[4:5]
	s_add_i32 m0, s24, 0x2000
	s_nop 0
	global_load_lds_dwordx4 v[6:7], off
.LBB0_1370:
	s_waitcnt lgkmcnt(5)
	v_mfma_f32_32x32x16_bf16 v[2:17], v[62:65], v[2:5], 0
	v_mfma_f32_32x32x16_bf16 v[18:33], v[62:65], v[18:21], 0
	v_mfma_f32_32x32x16_bf16 v[2:17], v[58:61], v[134:137], v[2:17]
	s_waitcnt lgkmcnt(4)
	v_mfma_f32_32x32x16_bf16 v[18:33], v[58:61], v[228:231], v[18:33]
	s_waitcnt lgkmcnt(3)
	v_mfma_f32_32x32x16_bf16 v[2:17], v[54:57], v[232:235], v[2:17]
	s_waitcnt lgkmcnt(2)
	v_mfma_f32_32x32x16_bf16 v[18:33], v[54:57], v[236:239], v[18:33]
	s_waitcnt lgkmcnt(1)
	v_mfma_f32_32x32x16_bf16 v[2:17], v[50:53], v[240:243], v[2:17]
	s_waitcnt lgkmcnt(0)
	v_mfma_f32_32x32x16_bf16 v[18:33], v[50:53], v[244:247], v[18:33]
	s_nop 9
	v_max_i32_e32 v166, 0, v2
	v_max_i32_e32 v136, 0, v10
	v_max_i32_e32 v2, 0, v3
	v_max_i32_e32 v10, 0, v11
	v_max_i32_e32 v167, 0, v18
	v_pk_fma_f32 v[134:135], v[74:75], v[166:167], 0 op_sel_hi:[1,1,0]
	v_max_i32_e32 v137, 0, v26
	v_max_i32_e32 v3, 0, v19
	v_pk_fma_f32 v[136:137], v[76:77], v[136:137], 0 op_sel_hi:[1,1,0]
	v_pk_fma_f32 v[2:3], v[46:47], v[2:3], v[134:135]
	v_max_i32_e32 v11, 0, v27
	v_max_i32_e32 v18, 0, v4
	v_max_i32_e32 v19, 0, v20
	v_pk_fma_f32 v[10:11], v[42:43], v[10:11], v[136:137]
	v_pk_fma_f32 v[2:3], v[78:79], v[18:19], v[2:3]
	v_max_i32_e32 v18, 0, v12
	v_max_i32_e32 v19, 0, v28
	v_max_i32_e32 v4, 0, v5
	v_max_i32_e32 v5, 0, v21
	v_pk_fma_f32 v[10:11], v[80:81], v[18:19], v[10:11]
	v_pk_fma_f32 v[2:3], v[48:49], v[4:5], v[2:3]
	v_max_i32_e32 v4, 0, v13
	v_max_i32_e32 v5, 0, v29
	v_pk_fma_f32 v[4:5], v[44:45], v[4:5], v[10:11]
	v_max_i32_e32 v10, 0, v6
	v_max_i32_e32 v11, 0, v22
	v_pk_fma_f32 v[2:3], v[82:83], v[10:11], v[2:3]
	v_max_i32_e32 v10, 0, v14
	v_max_i32_e32 v11, 0, v30
	v_max_i32_e32 v6, 0, v7
	v_max_i32_e32 v7, 0, v23
	v_pk_fma_f32 v[4:5], v[84:85], v[10:11], v[4:5]
	v_pk_fma_f32 v[2:3], v[38:39], v[6:7], v[2:3]
	v_max_i32_e32 v6, 0, v15
	v_max_i32_e32 v7, 0, v31
	v_pk_fma_f32 v[4:5], v[34:35], v[6:7], v[4:5]
	v_max_i32_e32 v6, 0, v8
	v_max_i32_e32 v7, 0, v24
	v_pk_fma_f32 v[2:3], v[86:87], v[6:7], v[2:3]
	v_max_i32_e32 v6, 0, v16
	v_max_i32_e32 v7, 0, v32
	v_pk_fma_f32 v[4:5], v[88:89], v[6:7], v[4:5]
	v_max_i32_e32 v6, 0, v9
	v_max_i32_e32 v7, 0, v25
	v_pk_fma_f32 v[2:3], v[40:41], v[6:7], v[2:3]
	v_max_i32_e32 v6, 0, v17
	v_max_i32_e32 v7, 0, v33
	v_pk_fma_f32 v[4:5], v[36:37], v[6:7], v[4:5]
	v_not_b32_e32 v6, v2
	v_or_b32_e32 v7, 0x80000000, v2
	v_cmp_gt_i32_e32 vcc, 0, v2
	v_not_b32_e32 v2, v3
	s_nop 0
	v_cndmask_b32_e32 v208, v7, v6, vcc
	v_or_b32_e32 v6, 0x80000000, v3
	v_cmp_gt_i32_e32 vcc, 0, v3
	v_or_b32_e32 v3, 0x80000000, v4
	s_nop 0
	v_cndmask_b32_e32 v141, v6, v2, vcc
	v_not_b32_e32 v2, v4
	v_cmp_gt_i32_e32 vcc, 0, v4
	v_permlane32_swap_b32_e32 v208, v141
	s_nop 0
	v_cndmask_b32_e32 v173, v3, v2, vcc
	v_not_b32_e32 v2, v5
	v_or_b32_e32 v3, 0x80000000, v5
	v_cmp_gt_i32_e32 vcc, 0, v5
	s_nop 1
	v_cndmask_b32_e32 v112, v3, v2, vcc
	s_nop 1
	v_permlane32_swap_b32_e32 v173, v112

.LBB0_1394:
	s_barrier
	ds_read_b128 v[2:5], v1 offset:24576
	ds_read_b128 v[18:21], v1 offset:28672
	ds_read_b128 v[134:137], v67 offset:24576
	ds_read_b128 v[228:231], v67 offset:28672
	ds_read_b128 v[232:235], v69 offset:24576
	ds_read_b128 v[236:239], v69 offset:28672
	ds_read_b128 v[240:243], v92 offset:24576
	ds_read_b128 v[244:247], v92 offset:28672
	s_cmp_lt_u32 s2, 52
	s_cbranch_scc1 .LBB0_1396
	s_mov_b64 s[4:5], 0x34000
	v_lshl_add_u64 v[6:7], v[90:91], 0, s[4:5]
	s_add_i32 m0, s24, 0x4000
	s_nop 0
	global_load_lds_dwordx4 v[6:7], off
.LBB0_1396:
	s_waitcnt lgkmcnt(5)
	v_mfma_f32_32x32x16_bf16 v[2:17], v[62:65], v[2:5], 0
	v_mfma_f32_32x32x16_bf16 v[18:33], v[62:65], v[18:21], 0
	v_mfma_f32_32x32x16_bf16 v[2:17], v[58:61], v[134:137], v[2:17]
	s_waitcnt lgkmcnt(4)
	v_mfma_f32_32x32x16_bf16 v[18:33], v[58:61], v[228:231], v[18:33]
	s_waitcnt lgkmcnt(3)
	v_mfma_f32_32x32x16_bf16 v[2:17], v[54:57], v[232:235], v[2:17]
	s_waitcnt lgkmcnt(2)
	v_mfma_f32_32x32x16_bf16 v[18:33], v[54:57], v[236:239], v[18:33]
	s_waitcnt lgkmcnt(1)
	v_mfma_f32_32x32x16_bf16 v[2:17], v[50:53], v[240:243], v[2:17]
	s_waitcnt lgkmcnt(0)
	v_mfma_f32_32x32x16_bf16 v[18:33], v[50:53], v[244:247], v[18:33]
	s_nop 9
	v_max_i32_e32 v166, 0, v2
	v_max_i32_e32 v136, 0, v10
	v_max_i32_e32 v2, 0, v3
	v_max_i32_e32 v10, 0, v11
	v_max_i32_e32 v167, 0, v18
	v_pk_fma_f32 v[134:135], v[74:75], v[166:167], 0 op_sel_hi:[1,1,0]
	v_max_i32_e32 v137, 0, v26
	v_max_i32_e32 v3, 0, v19
	v_pk_fma_f32 v[136:137], v[76:77], v[136:137], 0 op_sel_hi:[1,1,0]
	v_pk_fma_f32 v[2:3], v[46:47], v[2:3], v[134:135]
	v_max_i32_e32 v11, 0, v27
	v_max_i32_e32 v18, 0, v4
	v_max_i32_e32 v19, 0, v20
	v_pk_fma_f32 v[10:11], v[42:43], v[10:11], v[136:137]
	v_pk_fma_f32 v[2:3], v[78:79], v[18:19], v[2:3]
	v_max_i32_e32 v18, 0, v12
	v_max_i32_e32 v19, 0, v28
	v_max_i32_e32 v4, 0, v5
	v_max_i32_e32 v5, 0, v21
	v_pk_fma_f32 v[10:11], v[80:81], v[18:19], v[10:11]
	v_pk_fma_f32 v[2:3], v[48:49], v[4:5], v[2:3]
	v_max_i32_e32 v4, 0, v13
	v_max_i32_e32 v5, 0, v29
	v_pk_fma_f32 v[4:5], v[44:45], v[4:5], v[10:11]
	v_max_i32_e32 v10, 0, v6
	v_max_i32_e32 v11, 0, v22
	v_pk_fma_f32 v[2:3], v[82:83], v[10:11], v[2:3]
	v_max_i32_e32 v10, 0, v14
	v_max_i32_e32 v11, 0, v30
	v_max_i32_e32 v6, 0, v7
	v_max_i32_e32 v7, 0, v23
	v_pk_fma_f32 v[4:5], v[84:85], v[10:11], v[4:5]
	v_pk_fma_f32 v[2:3], v[38:39], v[6:7], v[2:3]
	v_max_i32_e32 v6, 0, v15
	v_max_i32_e32 v7, 0, v31
	v_pk_fma_f32 v[4:5], v[34:35], v[6:7], v[4:5]
	v_max_i32_e32 v6, 0, v8
	v_max_i32_e32 v7, 0, v24
	v_pk_fma_f32 v[2:3], v[86:87], v[6:7], v[2:3]
	v_max_i32_e32 v6, 0, v16
	v_max_i32_e32 v7, 0, v32
	v_pk_fma_f32 v[4:5], v[88:89], v[6:7], v[4:5]
	v_max_i32_e32 v6, 0, v9
	v_max_i32_e32 v7, 0, v25
	v_pk_fma_f32 v[2:3], v[40:41], v[6:7], v[2:3]
	v_max_i32_e32 v6, 0, v17
	v_max_i32_e32 v7, 0, v33
	v_pk_fma_f32 v[4:5], v[36:37], v[6:7], v[4:5]
	v_not_b32_e32 v6, v2
	v_or_b32_e32 v7, 0x80000000, v2
	v_cmp_gt_i32_e32 vcc, 0, v2
	v_not_b32_e32 v2, v3
	s_nop 0
	v_cndmask_b32_e32 v209, v7, v6, vcc
	v_or_b32_e32 v6, 0x80000000, v3
	v_cmp_gt_i32_e32 vcc, 0, v3
	v_or_b32_e32 v3, 0x80000000, v4
	s_nop 0
	v_cndmask_b32_e32 v143, v6, v2, vcc
	v_not_b32_e32 v2, v4
	v_cmp_gt_i32_e32 vcc, 0, v4
	v_permlane32_swap_b32_e32 v209, v143
	s_nop 0
	v_cndmask_b32_e32 v180, v3, v2, vcc
	v_not_b32_e32 v2, v5
	v_or_b32_e32 v3, 0x80000000, v5
	v_cmp_gt_i32_e32 vcc, 0, v5
	s_nop 1
	v_cndmask_b32_e32 v114, v3, v2, vcc
	s_nop 1
	v_permlane32_swap_b32_e32 v180, v114

.LBB0_1420:
	s_barrier
	ds_read_b128 v[2:5], v1 offset:32768
	ds_read_b128 v[18:21], v1 offset:36864
	ds_read_b128 v[134:137], v67 offset:32768
	ds_read_b128 v[228:231], v67 offset:36864
	ds_read_b128 v[232:235], v69 offset:32768
	ds_read_b128 v[236:239], v69 offset:36864
	ds_read_b128 v[240:243], v92 offset:32768
	ds_read_b128 v[244:247], v92 offset:36864
	s_cmp_lt_u32 s2, 54
	s_cbranch_scc1 .LBB0_1422
	s_mov_b64 s[4:5], 0x36000
	v_lshl_add_u64 v[6:7], v[90:91], 0, s[4:5]
	s_add_i32 m0, s24, 0x6000
	s_nop 0
	global_load_lds_dwordx4 v[6:7], off
.LBB0_1422:
	s_waitcnt lgkmcnt(5)
	v_mfma_f32_32x32x16_bf16 v[2:17], v[62:65], v[2:5], 0
	v_mfma_f32_32x32x16_bf16 v[18:33], v[62:65], v[18:21], 0
	v_mfma_f32_32x32x16_bf16 v[2:17], v[58:61], v[134:137], v[2:17]
	s_waitcnt lgkmcnt(4)
	v_mfma_f32_32x32x16_bf16 v[18:33], v[58:61], v[228:231], v[18:33]
	s_waitcnt lgkmcnt(3)
	v_mfma_f32_32x32x16_bf16 v[2:17], v[54:57], v[232:235], v[2:17]
	s_waitcnt lgkmcnt(2)
	v_mfma_f32_32x32x16_bf16 v[18:33], v[54:57], v[236:239], v[18:33]
	s_waitcnt lgkmcnt(1)
	v_mfma_f32_32x32x16_bf16 v[2:17], v[50:53], v[240:243], v[2:17]
	s_waitcnt lgkmcnt(0)
	v_mfma_f32_32x32x16_bf16 v[18:33], v[50:53], v[244:247], v[18:33]
	s_nop 9
	v_max_i32_e32 v166, 0, v2
	v_max_i32_e32 v136, 0, v10
	v_max_i32_e32 v2, 0, v3
	v_max_i32_e32 v10, 0, v11
	v_max_i32_e32 v167, 0, v18
	v_pk_fma_f32 v[134:135], v[74:75], v[166:167], 0 op_sel_hi:[1,1,0]
	v_max_i32_e32 v137, 0, v26
	v_max_i32_e32 v3, 0, v19
	v_pk_fma_f32 v[136:137], v[76:77], v[136:137], 0 op_sel_hi:[1,1,0]
	v_pk_fma_f32 v[2:3], v[46:47], v[2:3], v[134:135]
	v_max_i32_e32 v11, 0, v27
	v_max_i32_e32 v18, 0, v4
	v_max_i32_e32 v19, 0, v20
	v_pk_fma_f32 v[10:11], v[42:43], v[10:11], v[136:137]
	v_pk_fma_f32 v[2:3], v[78:79], v[18:19], v[2:3]
	v_max_i32_e32 v18, 0, v12
	v_max_i32_e32 v19, 0, v28
	v_max_i32_e32 v4, 0, v5
	v_max_i32_e32 v5, 0, v21
	v_pk_fma_f32 v[10:11], v[80:81], v[18:19], v[10:11]
	v_pk_fma_f32 v[2:3], v[48:49], v[4:5], v[2:3]
	v_max_i32_e32 v4, 0, v13
	v_max_i32_e32 v5, 0, v29
	v_pk_fma_f32 v[4:5], v[44:45], v[4:5], v[10:11]
	v_max_i32_e32 v10, 0, v6
	v_max_i32_e32 v11, 0, v22
	v_pk_fma_f32 v[2:3], v[82:83], v[10:11], v[2:3]
	v_max_i32_e32 v10, 0, v14
	v_max_i32_e32 v11, 0, v30
	v_max_i32_e32 v6, 0, v7
	v_max_i32_e32 v7, 0, v23
	v_pk_fma_f32 v[4:5], v[84:85], v[10:11], v[4:5]
	v_pk_fma_f32 v[2:3], v[38:39], v[6:7], v[2:3]
	v_max_i32_e32 v6, 0, v15
	v_max_i32_e32 v7, 0, v31
	v_pk_fma_f32 v[4:5], v[34:35], v[6:7], v[4:5]
	v_max_i32_e32 v6, 0, v8
	v_max_i32_e32 v7, 0, v24
	v_pk_fma_f32 v[2:3], v[86:87], v[6:7], v[2:3]
	v_max_i32_e32 v6, 0, v16
	v_max_i32_e32 v7, 0, v32
	v_pk_fma_f32 v[4:5], v[88:89], v[6:7], v[4:5]
	v_max_i32_e32 v6, 0, v9
	v_max_i32_e32 v7, 0, v25
	v_pk_fma_f32 v[2:3], v[40:41], v[6:7], v[2:3]
	v_max_i32_e32 v6, 0, v17
	v_max_i32_e32 v7, 0, v33
	v_pk_fma_f32 v[4:5], v[36:37], v[6:7], v[4:5]
	v_not_b32_e32 v6, v2
	v_or_b32_e32 v7, 0x80000000, v2
	v_cmp_gt_i32_e32 vcc, 0, v2
	v_not_b32_e32 v2, v3
	s_nop 0
	v_cndmask_b32_e32 v210, v7, v6, vcc
	v_or_b32_e32 v6, 0x80000000, v3
	v_cmp_gt_i32_e32 vcc, 0, v3
	v_or_b32_e32 v3, 0x80000000, v4
	s_nop 0
	v_cndmask_b32_e32 v145, v6, v2, vcc
	v_not_b32_e32 v2, v4
	v_cmp_gt_i32_e32 vcc, 0, v4
	v_permlane32_swap_b32_e32 v210, v145
	s_nop 0
	v_cndmask_b32_e32 v182, v3, v2, vcc
	v_not_b32_e32 v2, v5
	v_or_b32_e32 v3, 0x80000000, v5
	v_cmp_gt_i32_e32 vcc, 0, v5
	s_nop 1
	v_cndmask_b32_e32 v116, v3, v2, vcc
	s_nop 1
	v_permlane32_swap_b32_e32 v182, v116

.LBB0_1446:
	s_barrier
	ds_read_b128 v[2:5], v1 offset:40960
	ds_read_b128 v[18:21], v1 offset:45056
	ds_read_b128 v[134:137], v67 offset:40960
	ds_read_b128 v[228:231], v67 offset:45056
	ds_read_b128 v[232:235], v69 offset:40960
	ds_read_b128 v[236:239], v69 offset:45056
	ds_read_b128 v[240:243], v92 offset:40960
	ds_read_b128 v[244:247], v92 offset:45056
	s_cmp_lt_u32 s2, 56
	s_cbranch_scc1 .LBB0_1448
	s_mov_b64 s[4:5], 0x38000
	v_lshl_add_u64 v[6:7], v[90:91], 0, s[4:5]
	s_add_i32 m0, s24, 0x8000
	s_nop 0
	global_load_lds_dwordx4 v[6:7], off
.LBB0_1448:
	s_waitcnt lgkmcnt(5)
	v_mfma_f32_32x32x16_bf16 v[2:17], v[62:65], v[2:5], 0
	v_mfma_f32_32x32x16_bf16 v[18:33], v[62:65], v[18:21], 0
	v_mfma_f32_32x32x16_bf16 v[2:17], v[58:61], v[134:137], v[2:17]
	s_waitcnt lgkmcnt(4)
	v_mfma_f32_32x32x16_bf16 v[18:33], v[58:61], v[228:231], v[18:33]
	s_waitcnt lgkmcnt(3)
	v_mfma_f32_32x32x16_bf16 v[2:17], v[54:57], v[232:235], v[2:17]
	s_waitcnt lgkmcnt(2)
	v_mfma_f32_32x32x16_bf16 v[18:33], v[54:57], v[236:239], v[18:33]
	s_waitcnt lgkmcnt(1)
	v_mfma_f32_32x32x16_bf16 v[2:17], v[50:53], v[240:243], v[2:17]
	s_waitcnt lgkmcnt(0)
	v_mfma_f32_32x32x16_bf16 v[18:33], v[50:53], v[244:247], v[18:33]
	s_nop 9
	v_max_i32_e32 v166, 0, v2
	v_max_i32_e32 v136, 0, v10
	v_max_i32_e32 v2, 0, v3
	v_max_i32_e32 v10, 0, v11
	v_max_i32_e32 v167, 0, v18
	v_pk_fma_f32 v[134:135], v[74:75], v[166:167], 0 op_sel_hi:[1,1,0]
	v_max_i32_e32 v137, 0, v26
	v_max_i32_e32 v3, 0, v19
	v_pk_fma_f32 v[136:137], v[76:77], v[136:137], 0 op_sel_hi:[1,1,0]
	v_pk_fma_f32 v[2:3], v[46:47], v[2:3], v[134:135]
	v_max_i32_e32 v11, 0, v27
	v_max_i32_e32 v18, 0, v4
	v_max_i32_e32 v19, 0, v20
	v_pk_fma_f32 v[10:11], v[42:43], v[10:11], v[136:137]
	v_pk_fma_f32 v[2:3], v[78:79], v[18:19], v[2:3]
	v_max_i32_e32 v18, 0, v12
	v_max_i32_e32 v19, 0, v28
	v_max_i32_e32 v4, 0, v5
	v_max_i32_e32 v5, 0, v21
	v_pk_fma_f32 v[10:11], v[80:81], v[18:19], v[10:11]
	v_pk_fma_f32 v[2:3], v[48:49], v[4:5], v[2:3]
	v_max_i32_e32 v4, 0, v13
	v_max_i32_e32 v5, 0, v29
	v_pk_fma_f32 v[4:5], v[44:45], v[4:5], v[10:11]
	v_max_i32_e32 v10, 0, v6
	v_max_i32_e32 v11, 0, v22
	v_pk_fma_f32 v[2:3], v[82:83], v[10:11], v[2:3]
	v_max_i32_e32 v10, 0, v14
	v_max_i32_e32 v11, 0, v30
	v_max_i32_e32 v6, 0, v7
	v_max_i32_e32 v7, 0, v23
	v_pk_fma_f32 v[4:5], v[84:85], v[10:11], v[4:5]
	v_pk_fma_f32 v[2:3], v[38:39], v[6:7], v[2:3]
	v_max_i32_e32 v6, 0, v15
	v_max_i32_e32 v7, 0, v31
	v_pk_fma_f32 v[4:5], v[34:35], v[6:7], v[4:5]
	v_max_i32_e32 v6, 0, v8
	v_max_i32_e32 v7, 0, v24
	v_pk_fma_f32 v[2:3], v[86:87], v[6:7], v[2:3]
	v_max_i32_e32 v6, 0, v16
	v_max_i32_e32 v7, 0, v32
	v_pk_fma_f32 v[4:5], v[88:89], v[6:7], v[4:5]
	v_max_i32_e32 v6, 0, v9
	v_max_i32_e32 v7, 0, v25
	v_pk_fma_f32 v[2:3], v[40:41], v[6:7], v[2:3]
	v_max_i32_e32 v6, 0, v17
	v_max_i32_e32 v7, 0, v33
	v_pk_fma_f32 v[4:5], v[36:37], v[6:7], v[4:5]
	v_not_b32_e32 v6, v2
	v_or_b32_e32 v7, 0x80000000, v2
	v_cmp_gt_i32_e32 vcc, 0, v2
	v_not_b32_e32 v2, v3
	s_nop 0
	v_cndmask_b32_e32 v211, v7, v6, vcc
	v_or_b32_e32 v6, 0x80000000, v3
	v_cmp_gt_i32_e32 vcc, 0, v3
	v_or_b32_e32 v3, 0x80000000, v4
	s_nop 0
	v_cndmask_b32_e32 v147, v6, v2, vcc
	v_not_b32_e32 v2, v4
	v_cmp_gt_i32_e32 vcc, 0, v4
	v_permlane32_swap_b32_e32 v211, v147
	s_nop 0
	v_cndmask_b32_e32 v184, v3, v2, vcc
	v_not_b32_e32 v2, v5
	v_or_b32_e32 v3, 0x80000000, v5
	v_cmp_gt_i32_e32 vcc, 0, v5
	s_nop 1
	v_cndmask_b32_e32 v118, v3, v2, vcc
	s_nop 1
	v_permlane32_swap_b32_e32 v184, v118

.LBB0_1472:
	s_barrier
	ds_read_b128 v[2:5], v1 offset:49152
	ds_read_b128 v[18:21], v1 offset:53248
	ds_read_b128 v[134:137], v67 offset:49152
	ds_read_b128 v[228:231], v67 offset:53248
	ds_read_b128 v[232:235], v69 offset:49152
	ds_read_b128 v[236:239], v69 offset:53248
	ds_read_b128 v[240:243], v92 offset:49152
	ds_read_b128 v[244:247], v92 offset:53248
	s_cmp_lt_u32 s2, 58
	s_cbranch_scc1 .LBB0_1474
	s_mov_b64 s[4:5], 0x3a000
	v_lshl_add_u64 v[6:7], v[90:91], 0, s[4:5]
	s_add_i32 m0, s24, 0xa000
	s_nop 0
	global_load_lds_dwordx4 v[6:7], off
.LBB0_1474:
	s_waitcnt lgkmcnt(5)
	v_mfma_f32_32x32x16_bf16 v[2:17], v[62:65], v[2:5], 0
	v_mfma_f32_32x32x16_bf16 v[18:33], v[62:65], v[18:21], 0
	v_mfma_f32_32x32x16_bf16 v[2:17], v[58:61], v[134:137], v[2:17]
	s_waitcnt lgkmcnt(4)
	v_mfma_f32_32x32x16_bf16 v[18:33], v[58:61], v[228:231], v[18:33]
	s_waitcnt lgkmcnt(3)
	v_mfma_f32_32x32x16_bf16 v[2:17], v[54:57], v[232:235], v[2:17]
	s_waitcnt lgkmcnt(2)
	v_mfma_f32_32x32x16_bf16 v[18:33], v[54:57], v[236:239], v[18:33]
	s_waitcnt lgkmcnt(1)
	v_mfma_f32_32x32x16_bf16 v[2:17], v[50:53], v[240:243], v[2:17]
	s_waitcnt lgkmcnt(0)
	v_mfma_f32_32x32x16_bf16 v[18:33], v[50:53], v[244:247], v[18:33]
	s_nop 9
	v_max_i32_e32 v166, 0, v2
	v_max_i32_e32 v136, 0, v10
	v_max_i32_e32 v2, 0, v3
	v_max_i32_e32 v10, 0, v11
	v_max_i32_e32 v167, 0, v18
	v_pk_fma_f32 v[134:135], v[74:75], v[166:167], 0 op_sel_hi:[1,1,0]
	v_max_i32_e32 v137, 0, v26
	v_max_i32_e32 v3, 0, v19
	v_pk_fma_f32 v[136:137], v[76:77], v[136:137], 0 op_sel_hi:[1,1,0]
	v_pk_fma_f32 v[2:3], v[46:47], v[2:3], v[134:135]
	v_max_i32_e32 v11, 0, v27
	v_max_i32_e32 v18, 0, v4
	v_max_i32_e32 v19, 0, v20
	v_pk_fma_f32 v[10:11], v[42:43], v[10:11], v[136:137]
	v_pk_fma_f32 v[2:3], v[78:79], v[18:19], v[2:3]
	v_max_i32_e32 v18, 0, v12
	v_max_i32_e32 v19, 0, v28
	v_max_i32_e32 v4, 0, v5
	v_max_i32_e32 v5, 0, v21
	v_pk_fma_f32 v[10:11], v[80:81], v[18:19], v[10:11]
	v_pk_fma_f32 v[2:3], v[48:49], v[4:5], v[2:3]
	v_max_i32_e32 v4, 0, v13
	v_max_i32_e32 v5, 0, v29
	v_pk_fma_f32 v[4:5], v[44:45], v[4:5], v[10:11]
	v_max_i32_e32 v10, 0, v6
	v_max_i32_e32 v11, 0, v22
	v_pk_fma_f32 v[2:3], v[82:83], v[10:11], v[2:3]
	v_max_i32_e32 v10, 0, v14
	v_max_i32_e32 v11, 0, v30
	v_max_i32_e32 v6, 0, v7
	v_max_i32_e32 v7, 0, v23
	v_pk_fma_f32 v[4:5], v[84:85], v[10:11], v[4:5]
	v_pk_fma_f32 v[2:3], v[38:39], v[6:7], v[2:3]
	v_max_i32_e32 v6, 0, v15
	v_max_i32_e32 v7, 0, v31
	v_pk_fma_f32 v[4:5], v[34:35], v[6:7], v[4:5]
	v_max_i32_e32 v6, 0, v8
	v_max_i32_e32 v7, 0, v24
	v_pk_fma_f32 v[2:3], v[86:87], v[6:7], v[2:3]
	v_max_i32_e32 v6, 0, v16
	v_max_i32_e32 v7, 0, v32
	v_pk_fma_f32 v[4:5], v[88:89], v[6:7], v[4:5]
	v_max_i32_e32 v6, 0, v9
	v_max_i32_e32 v7, 0, v25
	v_pk_fma_f32 v[2:3], v[40:41], v[6:7], v[2:3]
	v_max_i32_e32 v6, 0, v17
	v_max_i32_e32 v7, 0, v33
	v_pk_fma_f32 v[4:5], v[36:37], v[6:7], v[4:5]
	v_not_b32_e32 v6, v2
	v_or_b32_e32 v7, 0x80000000, v2
	v_cmp_gt_i32_e32 vcc, 0, v2
	v_not_b32_e32 v2, v3
	s_nop 0
	v_cndmask_b32_e32 v212, v7, v6, vcc
	v_or_b32_e32 v6, 0x80000000, v3
	v_cmp_gt_i32_e32 vcc, 0, v3
	v_or_b32_e32 v3, 0x80000000, v4
	s_nop 0
	v_cndmask_b32_e32 v149, v6, v2, vcc
	v_not_b32_e32 v2, v4
	v_cmp_gt_i32_e32 vcc, 0, v4
	v_permlane32_swap_b32_e32 v212, v149
	s_nop 0
	v_cndmask_b32_e32 v186, v3, v2, vcc
	v_not_b32_e32 v2, v5
	v_or_b32_e32 v3, 0x80000000, v5
	v_cmp_gt_i32_e32 vcc, 0, v5
	s_nop 1
	v_cndmask_b32_e32 v120, v3, v2, vcc
	s_nop 1
	v_permlane32_swap_b32_e32 v186, v120

.LBB0_1498:
	s_barrier
	ds_read_b128 v[2:5], v1 offset:57344
	ds_read_b128 v[18:21], v1 offset:61440
	ds_read_b128 v[134:137], v67 offset:57344
	ds_read_b128 v[228:231], v67 offset:61440
	ds_read_b128 v[232:235], v69 offset:57344
	ds_read_b128 v[236:239], v69 offset:61440
	ds_read_b128 v[240:243], v92 offset:57344
	ds_read_b128 v[244:247], v92 offset:61440
	s_cmp_lt_u32 s2, 60
	s_cbranch_scc1 .LBB0_1500
	s_mov_b64 s[4:5], 0x3c000
	v_lshl_add_u64 v[6:7], v[90:91], 0, s[4:5]
	s_add_i32 m0, s24, 0xc000
	s_nop 0
	global_load_lds_dwordx4 v[6:7], off
.LBB0_1500:
	s_waitcnt lgkmcnt(5)
	v_mfma_f32_32x32x16_bf16 v[2:17], v[62:65], v[2:5], 0
	v_mfma_f32_32x32x16_bf16 v[18:33], v[62:65], v[18:21], 0
	v_mfma_f32_32x32x16_bf16 v[2:17], v[58:61], v[134:137], v[2:17]
	s_waitcnt lgkmcnt(4)
	v_mfma_f32_32x32x16_bf16 v[18:33], v[58:61], v[228:231], v[18:33]
	s_waitcnt lgkmcnt(3)
	v_mfma_f32_32x32x16_bf16 v[2:17], v[54:57], v[232:235], v[2:17]
	s_waitcnt lgkmcnt(2)
	v_mfma_f32_32x32x16_bf16 v[18:33], v[54:57], v[236:239], v[18:33]
	s_waitcnt lgkmcnt(1)
	v_mfma_f32_32x32x16_bf16 v[2:17], v[50:53], v[240:243], v[2:17]
	s_waitcnt lgkmcnt(0)
	v_mfma_f32_32x32x16_bf16 v[18:33], v[50:53], v[244:247], v[18:33]
	s_nop 9
	v_max_i32_e32 v166, 0, v2
	v_max_i32_e32 v136, 0, v10
	v_max_i32_e32 v2, 0, v3
	v_max_i32_e32 v10, 0, v11
	v_max_i32_e32 v167, 0, v18
	v_pk_fma_f32 v[134:135], v[74:75], v[166:167], 0 op_sel_hi:[1,1,0]
	v_max_i32_e32 v137, 0, v26
	v_max_i32_e32 v3, 0, v19
	v_pk_fma_f32 v[136:137], v[76:77], v[136:137], 0 op_sel_hi:[1,1,0]
	v_pk_fma_f32 v[2:3], v[46:47], v[2:3], v[134:135]
	v_max_i32_e32 v11, 0, v27
	v_max_i32_e32 v18, 0, v4
	v_max_i32_e32 v19, 0, v20
	v_pk_fma_f32 v[10:11], v[42:43], v[10:11], v[136:137]
	v_pk_fma_f32 v[2:3], v[78:79], v[18:19], v[2:3]
	v_max_i32_e32 v18, 0, v12
	v_max_i32_e32 v19, 0, v28
	v_max_i32_e32 v4, 0, v5
	v_max_i32_e32 v5, 0, v21
	v_pk_fma_f32 v[10:11], v[80:81], v[18:19], v[10:11]
	v_pk_fma_f32 v[2:3], v[48:49], v[4:5], v[2:3]
	v_max_i32_e32 v4, 0, v13
	v_max_i32_e32 v5, 0, v29
	v_pk_fma_f32 v[4:5], v[44:45], v[4:5], v[10:11]
	v_max_i32_e32 v10, 0, v6
	v_max_i32_e32 v11, 0, v22
	v_pk_fma_f32 v[2:3], v[82:83], v[10:11], v[2:3]
	v_max_i32_e32 v10, 0, v14
	v_max_i32_e32 v11, 0, v30
	v_max_i32_e32 v6, 0, v7
	v_max_i32_e32 v7, 0, v23
	v_pk_fma_f32 v[4:5], v[84:85], v[10:11], v[4:5]
	v_pk_fma_f32 v[2:3], v[38:39], v[6:7], v[2:3]
	v_max_i32_e32 v6, 0, v15
	v_max_i32_e32 v7, 0, v31
	v_pk_fma_f32 v[4:5], v[34:35], v[6:7], v[4:5]
	v_max_i32_e32 v6, 0, v8
	v_max_i32_e32 v7, 0, v24
	v_pk_fma_f32 v[2:3], v[86:87], v[6:7], v[2:3]
	v_max_i32_e32 v6, 0, v16
	v_max_i32_e32 v7, 0, v32
	v_pk_fma_f32 v[4:5], v[88:89], v[6:7], v[4:5]
	v_max_i32_e32 v6, 0, v9
	v_max_i32_e32 v7, 0, v25
	v_pk_fma_f32 v[2:3], v[40:41], v[6:7], v[2:3]
	v_max_i32_e32 v6, 0, v17
	v_max_i32_e32 v7, 0, v33
	v_pk_fma_f32 v[4:5], v[36:37], v[6:7], v[4:5]
	v_not_b32_e32 v6, v2
	v_or_b32_e32 v7, 0x80000000, v2
	v_cmp_gt_i32_e32 vcc, 0, v2
	v_not_b32_e32 v2, v3
	s_nop 0
	v_cndmask_b32_e32 v213, v7, v6, vcc
	v_or_b32_e32 v6, 0x80000000, v3
	v_cmp_gt_i32_e32 vcc, 0, v3
	v_or_b32_e32 v3, 0x80000000, v4
	s_nop 0
	v_cndmask_b32_e32 v151, v6, v2, vcc
	v_not_b32_e32 v2, v4
	v_cmp_gt_i32_e32 vcc, 0, v4
	v_permlane32_swap_b32_e32 v213, v151
	s_nop 0
	v_cndmask_b32_e32 v188, v3, v2, vcc
	v_not_b32_e32 v2, v5
	v_or_b32_e32 v3, 0x80000000, v5
	v_cmp_gt_i32_e32 vcc, 0, v5
	s_nop 1
	v_cndmask_b32_e32 v122, v3, v2, vcc
	s_nop 1
	v_permlane32_swap_b32_e32 v188, v122

.LBB0_1524:
	s_barrier
	ds_read_b128 v[2:5], v1
	ds_read_b128 v[18:21], v1 offset:4096
	ds_read_b128 v[134:137], v67
	ds_read_b128 v[228:231], v67 offset:4096
	ds_read_b128 v[232:235], v69
	ds_read_b128 v[236:239], v69 offset:4096
	ds_read_b128 v[240:243], v92
	ds_read_b128 v[244:247], v92 offset:4096
	s_cmp_lg_u32 s33, 31
	s_cbranch_scc1 .LBB0_1526
	s_mov_b64 s[4:5], 0x3e000
	v_lshl_add_u64 v[6:7], v[90:91], 0, s[4:5]
	s_add_i32 m0, s24, 0xe000
	s_nop 0
	global_load_lds_dwordx4 v[6:7], off
.LBB0_1526:
	s_waitcnt lgkmcnt(5)
	v_mfma_f32_32x32x16_bf16 v[2:17], v[62:65], v[2:5], 0
	v_mfma_f32_32x32x16_bf16 v[18:33], v[62:65], v[18:21], 0
	v_mfma_f32_32x32x16_bf16 v[2:17], v[58:61], v[134:137], v[2:17]
	s_waitcnt lgkmcnt(4)
	v_mfma_f32_32x32x16_bf16 v[18:33], v[58:61], v[228:231], v[18:33]
	s_waitcnt lgkmcnt(3)
	v_mfma_f32_32x32x16_bf16 v[2:17], v[54:57], v[232:235], v[2:17]
	s_waitcnt lgkmcnt(2)
	v_mfma_f32_32x32x16_bf16 v[18:33], v[54:57], v[236:239], v[18:33]
	s_waitcnt lgkmcnt(1)
	v_mfma_f32_32x32x16_bf16 v[2:17], v[50:53], v[240:243], v[2:17]
	s_waitcnt lgkmcnt(0)
	v_mfma_f32_32x32x16_bf16 v[18:33], v[50:53], v[244:247], v[18:33]
	s_nop 9
	v_max_i32_e32 v90, 0, v2
	v_max_i32_e32 v134, 0, v10
	v_max_i32_e32 v2, 0, v3
	v_max_i32_e32 v10, 0, v11
	v_max_i32_e32 v91, 0, v18
	v_pk_fma_f32 v[90:91], v[74:75], v[90:91], 0 op_sel_hi:[1,1,0]
	v_max_i32_e32 v135, 0, v26
	v_max_i32_e32 v3, 0, v19
	v_pk_fma_f32 v[134:135], v[76:77], v[134:135], 0 op_sel_hi:[1,1,0]
	v_pk_fma_f32 v[2:3], v[46:47], v[2:3], v[90:91]
	v_max_i32_e32 v11, 0, v27
	v_max_i32_e32 v18, 0, v4
	v_max_i32_e32 v19, 0, v20
	v_pk_fma_f32 v[10:11], v[42:43], v[10:11], v[134:135]
	v_pk_fma_f32 v[2:3], v[78:79], v[18:19], v[2:3]
	v_max_i32_e32 v18, 0, v12
	v_max_i32_e32 v19, 0, v28
	v_max_i32_e32 v4, 0, v5
	v_max_i32_e32 v5, 0, v21
	v_pk_fma_f32 v[10:11], v[80:81], v[18:19], v[10:11]
	v_pk_fma_f32 v[2:3], v[48:49], v[4:5], v[2:3]
	v_max_i32_e32 v4, 0, v13
	v_max_i32_e32 v5, 0, v29
	v_pk_fma_f32 v[4:5], v[44:45], v[4:5], v[10:11]
	v_max_i32_e32 v10, 0, v6
	v_max_i32_e32 v11, 0, v22
	v_pk_fma_f32 v[2:3], v[82:83], v[10:11], v[2:3]
	v_max_i32_e32 v10, 0, v14
	v_max_i32_e32 v11, 0, v30
	v_max_i32_e32 v6, 0, v7
	v_max_i32_e32 v7, 0, v23
	v_pk_fma_f32 v[4:5], v[84:85], v[10:11], v[4:5]
	v_pk_fma_f32 v[2:3], v[38:39], v[6:7], v[2:3]
	v_max_i32_e32 v6, 0, v15
	v_max_i32_e32 v7, 0, v31
	v_pk_fma_f32 v[4:5], v[34:35], v[6:7], v[4:5]
	v_max_i32_e32 v6, 0, v8
	v_max_i32_e32 v7, 0, v24
	v_pk_fma_f32 v[2:3], v[86:87], v[6:7], v[2:3]
	v_max_i32_e32 v6, 0, v16
	v_max_i32_e32 v7, 0, v32
	v_pk_fma_f32 v[4:5], v[88:89], v[6:7], v[4:5]
	v_max_i32_e32 v6, 0, v9
	v_max_i32_e32 v7, 0, v25
	v_pk_fma_f32 v[2:3], v[40:41], v[6:7], v[2:3]
	v_max_i32_e32 v6, 0, v17
	v_max_i32_e32 v7, 0, v33
	v_pk_fma_f32 v[4:5], v[36:37], v[6:7], v[4:5]
	v_not_b32_e32 v6, v2
	v_or_b32_e32 v7, 0x80000000, v2
	v_cmp_gt_i32_e32 vcc, 0, v2
	v_not_b32_e32 v2, v3
	s_nop 0
	v_cndmask_b32_e32 v214, v7, v6, vcc
	v_or_b32_e32 v6, 0x80000000, v3
	v_cmp_gt_i32_e32 vcc, 0, v3
	v_or_b32_e32 v3, 0x80000000, v4
	s_nop 0
	v_cndmask_b32_e32 v160, v6, v2, vcc
	v_not_b32_e32 v2, v4
	v_cmp_gt_i32_e32 vcc, 0, v4
	v_permlane32_swap_b32_e32 v214, v160
	s_nop 0
	v_cndmask_b32_e32 v197, v3, v2, vcc
	v_not_b32_e32 v2, v5
	v_or_b32_e32 v3, 0x80000000, v5
	v_cmp_gt_i32_e32 vcc, 0, v5
	s_nop 1
	v_cndmask_b32_e32 v131, v3, v2, vcc
	s_nop 1
	v_permlane32_swap_b32_e32 v197, v131
